# adds system-scope non-temporal hint (sc1 nt) on the weight-conversion f32 loads
# speedup vs baseline: 1.0244x; 1.0076x over previous
.LBB0_15:
	s_ashr_i32 s1, s0, 31
	s_lshl_b64 s[0:1], s[0:1], 10
	s_add_u32 s43, s10, s0
	s_addc_u32 s22, s12, s1
	s_lshl_b32 s0, s5, 6
	v_add_u32_e32 v48, s0, v1
	s_ashr_i32 s5, s4, 31
	v_lshl_add_u64 v[40:41], s[4:5], 2, v[36:37]
	s_movk_i32 s1, 0x5c00
	v_add_u32_e32 v46, 2, v48
	v_add_u32_e32 v50, 4, v48
	v_add_u32_e32 v52, 6, v48
	v_add_u32_e32 v54, 8, v48
	v_add_u32_e32 v56, 10, v48
	v_add_u32_e32 v58, 12, v48
	v_add_u32_e32 v60, 14, v48
	v_mad_i64_i32 v[44:45], s[4:5], v48, s1, v[40:41]
	v_mad_i64_i32 v[46:47], s[4:5], v46, s1, v[40:41]
	v_mad_i64_i32 v[50:51], s[4:5], v50, s1, v[40:41]
	v_mad_i64_i32 v[52:53], s[4:5], v52, s1, v[40:41]
	v_mad_i64_i32 v[54:55], s[4:5], v54, s1, v[40:41]
	v_mad_i64_i32 v[56:57], s[4:5], v56, s1, v[40:41]
	v_mad_i64_i32 v[58:59], s[4:5], v58, s1, v[40:41]
	v_mad_i64_i32 v[60:61], s[4:5], v60, s1, v[40:41]
	global_load_dword v62, v[44:45], off sc1 nt
	global_load_dword v63, v[46:47], off sc1 nt
	global_load_dword v64, v[50:51], off sc1 nt
	global_load_dword v65, v[52:53], off sc1 nt
	global_load_dword v66, v[54:55], off sc1 nt
	global_load_dword v67, v[56:57], off sc1 nt
	global_load_dword v68, v[58:59], off sc1 nt
	global_load_dword v69, v[60:61], off sc1 nt
	v_add_u32_e32 v44, 16, v48
	v_add_u32_e32 v46, 18, v48
	v_add_u32_e32 v50, 20, v48
	v_add_u32_e32 v52, 22, v48
	v_add_u32_e32 v54, 24, v48
	v_add_u32_e32 v56, 26, v48
	v_add_u32_e32 v58, 28, v48
	v_add_u32_e32 v60, 30, v48
	v_mad_i64_i32 v[44:45], s[4:5], v44, s1, v[40:41]
	v_mad_i64_i32 v[46:47], s[4:5], v46, s1, v[40:41]
	v_mad_i64_i32 v[50:51], s[4:5], v50, s1, v[40:41]
	v_mad_i64_i32 v[52:53], s[4:5], v52, s1, v[40:41]
	v_mad_i64_i32 v[54:55], s[4:5], v54, s1, v[40:41]
	v_mad_i64_i32 v[56:57], s[4:5], v56, s1, v[40:41]
	v_mad_i64_i32 v[58:59], s[4:5], v58, s1, v[40:41]
	v_mad_i64_i32 v[60:61], s[4:5], v60, s1, v[40:41]
	global_load_dword v70, v[44:45], off sc1 nt
	global_load_dword v71, v[46:47], off sc1 nt
	global_load_dword v72, v[50:51], off sc1 nt
	global_load_dword v73, v[52:53], off sc1 nt
	global_load_dword v74, v[54:55], off sc1 nt
	global_load_dword v75, v[56:57], off sc1 nt
	global_load_dword v76, v[58:59], off sc1 nt
	global_load_dword v77, v[60:61], off sc1 nt
	v_add_u32_e32 v44, 32, v48
	v_add_u32_e32 v46, 34, v48
	v_add_u32_e32 v50, 36, v48
	v_add_u32_e32 v52, 38, v48
	v_add_u32_e32 v54, 40, v48
	v_add_u32_e32 v56, 42, v48
	v_add_u32_e32 v58, 44, v48
	v_add_u32_e32 v60, 46, v48
	v_mad_i64_i32 v[44:45], s[4:5], v44, s1, v[40:41]
	v_mad_i64_i32 v[46:47], s[4:5], v46, s1, v[40:41]
	v_mad_i64_i32 v[50:51], s[4:5], v50, s1, v[40:41]
	v_mad_i64_i32 v[52:53], s[4:5], v52, s1, v[40:41]
	v_mad_i64_i32 v[54:55], s[4:5], v54, s1, v[40:41]
	v_mad_i64_i32 v[56:57], s[4:5], v56, s1, v[40:41]
	v_mad_i64_i32 v[58:59], s[4:5], v58, s1, v[40:41]
	v_mad_i64_i32 v[60:61], s[4:5], v60, s1, v[40:41]
	global_load_dword v78, v[44:45], off sc1 nt
	global_load_dword v79, v[46:47], off sc1 nt
	global_load_dword v80, v[50:51], off sc1 nt
	global_load_dword v81, v[52:53], off sc1 nt
	global_load_dword v82, v[54:55], off sc1 nt
	global_load_dword v83, v[56:57], off sc1 nt
	global_load_dword v84, v[58:59], off sc1 nt
	s_nop 0
	global_load_dword v60, v[60:61], off sc1 nt
	v_add_u32_e32 v44, 48, v48
	v_add_u32_e32 v46, 50, v48
	v_add_u32_e32 v50, 52, v48
	v_add_u32_e32 v52, 54, v48
	v_add_u32_e32 v54, 56, v48
	v_add_u32_e32 v56, 58, v48
	v_add_u32_e32 v58, 60, v48
	v_add_u32_e32 v48, 62, v48
	v_mad_i64_i32 v[44:45], s[4:5], v44, s1, v[40:41]
	v_mad_i64_i32 v[46:47], s[4:5], v46, s1, v[40:41]
	v_mad_i64_i32 v[50:51], s[4:5], v50, s1, v[40:41]
	v_mad_i64_i32 v[52:53], s[4:5], v52, s1, v[40:41]
	v_mad_i64_i32 v[54:55], s[4:5], v54, s1, v[40:41]
	v_mad_i64_i32 v[56:57], s[4:5], v56, s1, v[40:41]
	v_mad_i64_i32 v[58:59], s[4:5], v58, s1, v[40:41]
	v_mad_i64_i32 v[40:41], s[4:5], v48, s1, v[40:41]
	global_load_dword v44, v[44:45], off sc1 nt
	s_nop 0
	global_load_dword v45, v[46:47], off sc1 nt
	s_nop 0
	global_load_dword v46, v[50:51], off sc1 nt
	global_load_dword v47, v[52:53], off sc1 nt
	global_load_dword v48, v[54:55], off sc1 nt
	s_nop 0
	global_load_dword v50, v[56:57], off sc1 nt
	global_load_dword v51, v[58:59], off sc1 nt
	s_nop 0
	global_load_dword v40, v[40:41], off sc1 nt
	v_add_u32_e32 v41, 0x400, v42
	s_waitcnt vmcnt(30)
	ds_write2_b32 v42, v62, v63 offset1:66
	s_waitcnt vmcnt(28)
	ds_write2_b32 v42, v64, v65 offset0:132 offset1:198
	s_waitcnt vmcnt(26)
	ds_write2_b32 v41, v66, v67 offset0:8 offset1:74
	s_waitcnt vmcnt(24)
	ds_write2_b32 v41, v68, v69 offset0:140 offset1:206
	v_add_u32_e32 v41, 0x800, v42
	s_waitcnt vmcnt(22)
	ds_write2_b32 v41, v70, v71 offset0:16 offset1:82
	s_waitcnt vmcnt(20)
	ds_write2_b32 v41, v72, v73 offset0:148 offset1:214
	v_add_u32_e32 v41, 0xc00, v42
	s_waitcnt vmcnt(18)
	ds_write2_b32 v41, v74, v75 offset0:24 offset1:90
	s_waitcnt vmcnt(16)
	ds_write2_b32 v41, v76, v77 offset0:156 offset1:222
	v_add_u32_e32 v41, 0x1000, v42
	s_waitcnt vmcnt(14)
	ds_write2_b32 v41, v78, v79 offset0:32 offset1:98
	s_waitcnt vmcnt(12)
	ds_write2_b32 v41, v80, v81 offset0:164 offset1:230
	v_add_u32_e32 v41, 0x1400, v42
	s_waitcnt vmcnt(10)
	ds_write2_b32 v41, v82, v83 offset0:40 offset1:106
	s_waitcnt vmcnt(8)
	ds_write2_b32 v41, v84, v60 offset0:172 offset1:238
	v_add_u32_e32 v41, 0x1800, v42
	s_waitcnt vmcnt(6)
	ds_write2_b32 v41, v44, v45 offset0:48 offset1:114
	s_waitcnt vmcnt(4)
	ds_write2_b32 v41, v46, v47 offset0:180 offset1:246
	v_add_u32_e32 v41, 0x1c00, v42
	s_waitcnt vmcnt(2)
	ds_write2_b32 v41, v48, v50 offset0:56 offset1:122
	s_waitcnt vmcnt(0)
	ds_write2_b32 v41, v51, v40 offset0:188 offset1:254
	s_waitcnt lgkmcnt(0)
	s_ashr_i32 s1, s0, 31
	v_lshl_add_u64 v[40:41], s[0:1], 2, v[38:39]
	global_load_dwordx4 v[44:47], v[40:41], off
	global_load_dwordx4 v[50:53], v[40:41], off offset:16
	ds_read2_b32 v[40:41], v43 offset1:8
	ds_read2_b32 v[54:55], v43 offset0:33 offset1:41
	ds_read2_b32 v[56:57], v43 offset0:66 offset1:74
	s_mov_b32 s4, 0x42800000
	ds_read2_b32 v[58:59], v43 offset0:99 offset1:107
	v_mov_b32_e32 v60, v49
	ds_read2_b32 v[62:63], v43 offset0:132 offset1:140
	ds_read2_b32 v[64:65], v43 offset0:165 offset1:173
	ds_read2_b32 v[66:67], v43 offset0:198 offset1:206
	ds_read2_b32 v[68:69], v43 offset0:231 offset1:239
	v_mov_b32_e32 v61, v49
	s_add_u32 s0, s43, s0
	s_addc_u32 s1, s22, s1
	v_lshl_add_u64 v[70:71], s[0:1], 0, v[2:3]
	v_lshl_add_u64 v[72:73], v[70:71], 0, v[4:5]
	s_waitcnt vmcnt(1)
	v_pk_mul_f32 v[44:45], v[44:45], s[4:5] op_sel_hi:[1,0]
	s_waitcnt lgkmcnt(7)
	v_mul_f32_e32 v40, v44, v40
	s_waitcnt lgkmcnt(6)
	v_mul_f32_e32 v48, v45, v54
	v_med3_f32 v40, v40, s11, v232
	v_med3_f32 v48, v48, s11, v232
	v_cvt_pk_fp8_f32 v60, v40, v48
	v_pk_mul_f32 v[46:47], v[46:47], s[4:5] op_sel_hi:[1,0]
	s_waitcnt vmcnt(0)
	v_pk_mul_f32 v[50:51], v[50:51], s[4:5] op_sel_hi:[1,0]
	s_waitcnt lgkmcnt(5)
	v_mul_f32_e32 v54, v46, v56
	s_waitcnt lgkmcnt(4)
	v_mul_f32_e32 v56, v47, v58
	v_med3_f32 v40, v54, s11, v232
	v_med3_f32 v48, v56, s11, v232
	v_cvt_pk_fp8_f32 v60, v40, v48 op_sel:[0,0,1]
	s_waitcnt lgkmcnt(3)
	v_mul_f32_e32 v40, v50, v62
	s_waitcnt lgkmcnt(2)
	v_mul_f32_e32 v48, v51, v64
	v_med3_f32 v40, v40, s11, v232
	v_med3_f32 v48, v48, s11, v232
	v_cvt_pk_fp8_f32 v61, v40, v48
	v_pk_mul_f32 v[52:53], v[52:53], s[4:5] op_sel_hi:[1,0]
	s_waitcnt lgkmcnt(1)
	v_mul_f32_e32 v54, v52, v66
	s_waitcnt lgkmcnt(0)
	v_mul_f32_e32 v40, v53, v68
	v_med3_f32 v48, v54, s11, v232
	v_med3_f32 v40, v40, s11, v232
	v_cvt_pk_fp8_f32 v61, v48, v40 op_sel:[0,0,1]
	v_mul_f32_e32 v40, v44, v41
	v_mul_f32_e32 v41, v45, v55
	v_med3_f32 v54, v40, s11, v232
	v_med3_f32 v41, v41, s11, v232
	v_mov_b32_e32 v40, v49
	v_cvt_pk_fp8_f32 v40, v54, v41
	v_mul_f32_e32 v48, v46, v57
	v_mul_f32_e32 v41, v47, v59
	v_med3_f32 v48, v48, s11, v232
	v_med3_f32 v41, v41, s11, v232
	v_cvt_pk_fp8_f32 v40, v48, v41 op_sel:[0,0,1]
	v_mul_f32_e32 v41, v50, v63
	v_mul_f32_e32 v48, v51, v65
	v_med3_f32 v55, v41, s11, v232
	v_med3_f32 v48, v48, s11, v232
	v_mov_b32_e32 v41, v49
	v_cvt_pk_fp8_f32 v41, v55, v48
	v_mul_f32_e32 v54, v52, v67
	v_mul_f32_e32 v48, v53, v69
	v_med3_f32 v54, v54, s11, v232
	v_med3_f32 v48, v48, s11, v232
	global_store_dwordx2 v[72:73], v[60:61], off
	v_cvt_pk_fp8_f32 v41, v54, v48 op_sel:[0,0,1]
	ds_read2_b32 v[56:57], v43 offset0:16 offset1:24
	ds_read2_b32 v[58:59], v43 offset0:49 offset1:57
	ds_read2_b32 v[60:61], v43 offset0:82 offset1:90
	ds_read2_b32 v[62:63], v43 offset0:115 offset1:123
	v_lshl_add_u64 v[54:55], v[70:71], 0, v[6:7]
	global_store_dwordx2 v[54:55], v[40:41], off
	s_waitcnt lgkmcnt(3)
	v_mul_f32_e32 v40, v44, v56
	s_waitcnt lgkmcnt(2)
	v_mul_f32_e32 v41, v45, v58
	v_med3_f32 v54, v40, s11, v232
	v_med3_f32 v41, v41, s11, v232
	v_mov_b32_e32 v40, v49
	v_cvt_pk_fp8_f32 v40, v54, v41
	ds_read2_b32 v[54:55], v43 offset0:148 offset1:156
	ds_read2_b32 v[64:65], v43 offset0:181 offset1:189
	ds_read2_b32 v[66:67], v43 offset0:214 offset1:222
	s_waitcnt lgkmcnt(4)
	v_mul_f32_e32 v48, v46, v60
	s_waitcnt lgkmcnt(3)
	v_mul_f32_e32 v56, v47, v62
	v_med3_f32 v41, v48, s11, v232
	v_med3_f32 v48, v56, s11, v232
	ds_read2_b32 v[68:69], v43 offset0:247 offset1:255
	v_cvt_pk_fp8_f32 v40, v41, v48 op_sel:[0,0,1]
	s_waitcnt lgkmcnt(3)
	v_mul_f32_e32 v41, v50, v54
	s_waitcnt lgkmcnt(2)
	v_mul_f32_e32 v48, v51, v64
	v_med3_f32 v56, v41, s11, v232
	v_med3_f32 v48, v48, s11, v232
	v_mov_b32_e32 v41, v49
	v_cvt_pk_fp8_f32 v41, v56, v48
	s_waitcnt lgkmcnt(1)
	v_mul_f32_e32 v54, v52, v66
	s_waitcnt lgkmcnt(0)
	v_mul_f32_e32 v48, v53, v68
	v_med3_f32 v54, v54, s11, v232
	v_med3_f32 v48, v48, s11, v232
	v_mul_f32_e32 v44, v44, v57
	v_mul_f32_e32 v45, v45, v59
	v_cvt_pk_fp8_f32 v41, v54, v48 op_sel:[0,0,1]
	v_med3_f32 v48, v44, s11, v232
	v_med3_f32 v45, v45, s11, v232
	v_mov_b32_e32 v44, v49
	v_cvt_pk_fp8_f32 v44, v48, v45
	v_mul_f32_e32 v46, v46, v61
	v_mul_f32_e32 v45, v47, v63
	v_med3_f32 v46, v46, s11, v232
	v_med3_f32 v45, v45, s11, v232
	v_cvt_pk_fp8_f32 v44, v46, v45 op_sel:[0,0,1]
	v_mul_f32_e32 v45, v50, v55
	v_mul_f32_e32 v46, v51, v65
	v_med3_f32 v48, v45, s11, v232
	v_med3_f32 v46, v46, s11, v232
	v_mov_b32_e32 v45, v49
	v_cvt_pk_fp8_f32 v45, v48, v46
	v_mul_f32_e32 v47, v52, v67
	v_mul_f32_e32 v46, v53, v69
	v_med3_f32 v47, v47, s11, v232
	v_med3_f32 v46, v46, s11, v232
	v_cvt_pk_fp8_f32 v45, v47, v46 op_sel:[0,0,1]
	v_lshl_add_u64 v[46:47], v[70:71], 0, v[8:9]
	global_store_dwordx2 v[46:47], v[40:41], off
	v_lshl_add_u64 v[40:41], v[70:71], 0, v[10:11]
	global_store_dwordx2 v[40:41], v[44:45], off
	s_waitcnt lgkmcnt(0)

.LBB0_17:
	s_cmpk_gt_i32 s42, 0xb7f
	s_mov_b64 s[0:1], -1
	s_cbranch_scc0 .LBB0_35
	s_cmpk_gt_u32 s42, 0xbff
	s_cbranch_scc0 .LBB0_32
	s_cmpk_gt_u32 s42, 0xdff
	s_cbranch_scc0 .LBB0_29
	s_cmpk_gt_u32 s42, 0xfff
	s_cbranch_scc0 .LBB0_26
	s_cmpk_gt_u32 s42, 0x4fff
	v_lshlrev_b32_e32 v48, 2, v0
	s_cbranch_scc0 .LBB0_23
	s_add_i32 s0, s42, 0xffffb000
	s_lshr_b32 s22, s0, 9
	s_lshl_b64 s[0:1], s[22:23], 22
	s_add_u32 s5, s36, s0
	s_addc_u32 s43, s37, s1
	s_and_b32 s44, s39, 0x3e0
	s_lshl_b64 s[0:1], s[22:23], 20
	s_lshl_b32 s4, s44, 10
	s_add_u32 s0, s31, s0
	s_addc_u32 s22, s33, s1
	s_add_u32 s1, s0, s4
	s_addc_u32 s0, s22, 0
	s_and_b32 s4, s41, 0x3c0
	s_lshl_b32 s22, s44, 2
	v_add_u32_e32 v40, s4, v1
	s_add_u32 s44, s5, s22
	s_addc_u32 s45, s43, 0
	v_ashrrev_i32_e32 v41, 31, v40
	v_lshl_add_u64 v[44:45], s[44:45], 0, v[48:49]
	v_lshlrev_b64 v[40:41], 12, v[40:41]
	v_lshl_add_u64 v[40:41], v[44:45], 0, v[40:41]
	s_movk_i32 s5, 0x2000
	v_add_co_u32_e32 v44, vcc, s5, v40
	s_movk_i32 s5, 0x4000
	s_nop 0
	v_addc_co_u32_e32 v45, vcc, 0, v41, vcc
	v_add_co_u32_e32 v46, vcc, s5, v40
	s_movk_i32 s5, 0x6000
	s_nop 0
	v_addc_co_u32_e32 v47, vcc, 0, v41, vcc
	v_add_co_u32_e32 v50, vcc, s5, v40
	s_mov_b32 s5, 0x8000
	s_nop 0
	v_addc_co_u32_e32 v51, vcc, 0, v41, vcc
	v_add_co_u32_e32 v52, vcc, s5, v40
	s_mov_b32 s5, 0xa000
	s_nop 0
	v_addc_co_u32_e32 v53, vcc, 0, v41, vcc
	v_add_co_u32_e32 v54, vcc, s5, v40
	s_mov_b32 s5, 0xc000
	s_nop 0
	v_addc_co_u32_e32 v55, vcc, 0, v41, vcc
	v_add_co_u32_e32 v56, vcc, s5, v40
	s_mov_b32 s5, 0xe000
	s_nop 0
	v_addc_co_u32_e32 v57, vcc, 0, v41, vcc
	v_add_co_u32_e32 v58, vcc, s5, v40
	s_mov_b32 s5, 0x10000
	s_nop 0
	v_addc_co_u32_e32 v59, vcc, 0, v41, vcc
	global_load_dword v62, v[40:41], off sc1 nt
	global_load_dword v63, v[44:45], off sc1 nt
	global_load_dword v64, v[46:47], off sc1 nt
	global_load_dword v65, v[50:51], off sc1 nt
	global_load_dword v66, v[52:53], off sc1 nt
	global_load_dword v67, v[54:55], off sc1 nt
	global_load_dword v68, v[56:57], off sc1 nt
	global_load_dword v69, v[58:59], off sc1 nt
	v_add_co_u32_e32 v44, vcc, s5, v40
	s_mov_b32 s5, 0x12000
	s_nop 0
	v_addc_co_u32_e32 v45, vcc, 0, v41, vcc
	v_add_co_u32_e32 v46, vcc, s5, v40
	s_mov_b32 s5, 0x14000
	s_nop 0
	v_addc_co_u32_e32 v47, vcc, 0, v41, vcc
	v_add_co_u32_e32 v50, vcc, s5, v40
	s_mov_b32 s5, 0x16000
	s_nop 0
	v_addc_co_u32_e32 v51, vcc, 0, v41, vcc
	v_add_co_u32_e32 v52, vcc, s5, v40
	s_mov_b32 s5, 0x18000
	s_nop 0
	v_addc_co_u32_e32 v53, vcc, 0, v41, vcc
	v_add_co_u32_e32 v54, vcc, s5, v40
	s_mov_b32 s5, 0x1a000
	s_nop 0
	v_addc_co_u32_e32 v55, vcc, 0, v41, vcc
	v_add_co_u32_e32 v56, vcc, s5, v40
	s_mov_b32 s5, 0x1c000
	s_nop 0
	v_addc_co_u32_e32 v57, vcc, 0, v41, vcc
	v_add_co_u32_e32 v58, vcc, s5, v40
	s_mov_b32 s5, 0x1e000
	s_nop 0
	v_addc_co_u32_e32 v59, vcc, 0, v41, vcc
	v_add_co_u32_e32 v60, vcc, s5, v40
	s_mov_b32 s5, 0x20000
	s_nop 0
	v_addc_co_u32_e32 v61, vcc, 0, v41, vcc
	global_load_dword v70, v[44:45], off sc1 nt
	global_load_dword v71, v[46:47], off sc1 nt
	global_load_dword v72, v[50:51], off sc1 nt
	global_load_dword v73, v[52:53], off sc1 nt
	global_load_dword v74, v[54:55], off sc1 nt
	global_load_dword v75, v[56:57], off sc1 nt
	global_load_dword v76, v[58:59], off sc1 nt
	global_load_dword v77, v[60:61], off sc1 nt
	v_add_co_u32_e32 v44, vcc, s5, v40
	s_mov_b32 s5, 0x22000
	s_nop 0
	v_addc_co_u32_e32 v45, vcc, 0, v41, vcc
	v_add_co_u32_e32 v46, vcc, s5, v40
	s_mov_b32 s5, 0x24000
	s_nop 0
	v_addc_co_u32_e32 v47, vcc, 0, v41, vcc
	v_add_co_u32_e32 v50, vcc, s5, v40
	s_mov_b32 s5, 0x26000
	s_nop 0
	v_addc_co_u32_e32 v51, vcc, 0, v41, vcc
	v_add_co_u32_e32 v52, vcc, s5, v40
	s_mov_b32 s5, 0x28000
	s_nop 0
	v_addc_co_u32_e32 v53, vcc, 0, v41, vcc
	v_add_co_u32_e32 v54, vcc, s5, v40
	s_mov_b32 s5, 0x2a000
	s_nop 0
	v_addc_co_u32_e32 v55, vcc, 0, v41, vcc
	v_add_co_u32_e32 v56, vcc, s5, v40
	s_mov_b32 s5, 0x2c000
	s_nop 0
	v_addc_co_u32_e32 v57, vcc, 0, v41, vcc
	v_add_co_u32_e32 v58, vcc, s5, v40
	s_mov_b32 s5, 0x2e000
	s_nop 0
	v_addc_co_u32_e32 v59, vcc, 0, v41, vcc
	v_add_co_u32_e32 v60, vcc, s5, v40
	s_mov_b32 s5, 0x30000
	s_nop 0
	v_addc_co_u32_e32 v61, vcc, 0, v41, vcc
	global_load_dword v78, v[44:45], off sc1 nt
	global_load_dword v79, v[46:47], off sc1 nt
	global_load_dword v80, v[50:51], off sc1 nt
	global_load_dword v81, v[52:53], off sc1 nt
	global_load_dword v82, v[54:55], off sc1 nt
	global_load_dword v83, v[56:57], off sc1 nt
	global_load_dword v84, v[58:59], off sc1 nt
	s_nop 0
	global_load_dword v60, v[60:61], off sc1 nt
	v_add_co_u32_e32 v44, vcc, s5, v40
	s_mov_b32 s5, 0x32000
	s_nop 0
	v_addc_co_u32_e32 v45, vcc, 0, v41, vcc
	v_add_co_u32_e32 v46, vcc, s5, v40
	s_mov_b32 s5, 0x34000
	s_nop 0
	v_addc_co_u32_e32 v47, vcc, 0, v41, vcc
	v_add_co_u32_e32 v50, vcc, s5, v40
	s_mov_b32 s5, 0x36000
	s_nop 0
	v_addc_co_u32_e32 v51, vcc, 0, v41, vcc
	v_add_co_u32_e32 v52, vcc, s5, v40
	s_mov_b32 s5, 0x38000
	s_nop 0
	v_addc_co_u32_e32 v53, vcc, 0, v41, vcc
	v_add_co_u32_e32 v54, vcc, s5, v40
	s_mov_b32 s5, 0x3a000
	s_nop 0
	v_addc_co_u32_e32 v55, vcc, 0, v41, vcc
	v_add_co_u32_e32 v56, vcc, s5, v40
	s_mov_b32 s5, 0x3c000
	s_nop 0
	v_addc_co_u32_e32 v57, vcc, 0, v41, vcc
	v_add_co_u32_e32 v58, vcc, s5, v40
	s_mov_b32 s5, 0x3e000
	s_nop 0
	v_addc_co_u32_e32 v59, vcc, 0, v41, vcc
	v_add_co_u32_e32 v40, vcc, s5, v40
	s_add_u32 s4, s1, s4
	s_nop 0
	v_addc_co_u32_e32 v41, vcc, 0, v41, vcc
	global_load_dword v44, v[44:45], off sc1 nt
	s_nop 0
	global_load_dword v45, v[46:47], off sc1 nt
	s_nop 0
	global_load_dword v46, v[50:51], off sc1 nt
	global_load_dword v47, v[52:53], off sc1 nt
	s_nop 0
	global_load_dword v50, v[54:55], off sc1 nt
	global_load_dword v51, v[56:57], off sc1 nt
	global_load_dword v52, v[58:59], off sc1 nt
	s_nop 0
	global_load_dword v40, v[40:41], off sc1 nt
	v_add_u32_e32 v41, 0x400, v42
	s_waitcnt vmcnt(30)
	ds_write2_b32 v42, v62, v63 offset1:66
	s_waitcnt vmcnt(28)
	ds_write2_b32 v42, v64, v65 offset0:132 offset1:198
	s_waitcnt vmcnt(26)
	ds_write2_b32 v41, v66, v67 offset0:8 offset1:74
	s_waitcnt vmcnt(24)
	ds_write2_b32 v41, v68, v69 offset0:140 offset1:206
	v_add_u32_e32 v41, 0x800, v42
	s_waitcnt vmcnt(22)
	ds_write2_b32 v41, v70, v71 offset0:16 offset1:82
	s_waitcnt vmcnt(20)
	ds_write2_b32 v41, v72, v73 offset0:148 offset1:214
	v_add_u32_e32 v41, 0xc00, v42
	s_waitcnt vmcnt(18)
	ds_write2_b32 v41, v74, v75 offset0:24 offset1:90
	s_waitcnt vmcnt(16)
	ds_write2_b32 v41, v76, v77 offset0:156 offset1:222
	v_add_u32_e32 v41, 0x1000, v42
	s_waitcnt vmcnt(14)
	ds_write2_b32 v41, v78, v79 offset0:32 offset1:98
	s_waitcnt vmcnt(12)
	ds_write2_b32 v41, v80, v81 offset0:164 offset1:230
	v_add_u32_e32 v41, 0x1400, v42
	s_waitcnt vmcnt(10)
	ds_write2_b32 v41, v82, v83 offset0:40 offset1:106
	s_waitcnt vmcnt(8)
	ds_write2_b32 v41, v84, v60 offset0:172 offset1:238
	v_add_u32_e32 v41, 0x1800, v42
	s_waitcnt vmcnt(6)
	ds_write2_b32 v41, v44, v45 offset0:48 offset1:114
	s_waitcnt vmcnt(4)
	ds_write2_b32 v41, v46, v47 offset0:180 offset1:246
	v_add_u32_e32 v41, 0x1c00, v42
	s_waitcnt vmcnt(2)
	ds_write2_b32 v41, v50, v51 offset0:56 offset1:122
	s_waitcnt vmcnt(0)
	ds_write2_b32 v41, v52, v40 offset0:188 offset1:254
	s_waitcnt lgkmcnt(0)
	ds_read2_b32 v[40:41], v43 offset1:8
	ds_read2_b32 v[44:45], v43 offset0:33 offset1:41
	ds_read2_b32 v[46:47], v43 offset0:66 offset1:74
	ds_read2_b32 v[50:51], v43 offset0:99 offset1:107
	v_mov_b32_e32 v52, v49
	s_waitcnt lgkmcnt(3)
	v_mul_f32_e32 v40, 0x42800000, v40
	s_waitcnt lgkmcnt(2)
	v_mul_f32_e32 v44, 0x42800000, v44
	v_med3_f32 v40, v40, s11, v232
	v_med3_f32 v44, v44, s11, v232
	v_cvt_pk_fp8_f32 v52, v40, v44
	ds_read2_b32 v[54:55], v43 offset0:132 offset1:140
	ds_read2_b32 v[56:57], v43 offset0:165 offset1:173
	ds_read2_b32 v[58:59], v43 offset0:198 offset1:206
	s_waitcnt lgkmcnt(4)
	v_mul_f32_e32 v46, 0x42800000, v46
	s_waitcnt lgkmcnt(3)
	v_mul_f32_e32 v50, 0x42800000, v50
	v_med3_f32 v40, v46, s11, v232
	v_med3_f32 v44, v50, s11, v232
	ds_read2_b32 v[60:61], v43 offset0:231 offset1:239
	v_cvt_pk_fp8_f32 v52, v40, v44 op_sel:[0,0,1]
	s_waitcnt lgkmcnt(3)
	v_mul_f32_e32 v40, 0x42800000, v54
	s_waitcnt lgkmcnt(2)
	v_mul_f32_e32 v44, 0x42800000, v56
	v_med3_f32 v40, v40, s11, v232
	v_med3_f32 v44, v44, s11, v232
	v_mov_b32_e32 v53, v49
	v_cvt_pk_fp8_f32 v53, v40, v44
	s_waitcnt lgkmcnt(1)
	v_mul_f32_e32 v46, 0x42800000, v58
	s_waitcnt lgkmcnt(0)
	v_mul_f32_e32 v40, 0x42800000, v60
	v_med3_f32 v44, v46, s11, v232
	v_med3_f32 v40, v40, s11, v232
	v_cvt_pk_fp8_f32 v53, v44, v40 op_sel:[0,0,1]
	v_mul_f32_e32 v40, 0x42800000, v41
	v_mul_f32_e32 v41, 0x42800000, v45
	v_med3_f32 v45, v40, s11, v232
	v_med3_f32 v41, v41, s11, v232
	v_mov_b32_e32 v40, v49
	v_cvt_pk_fp8_f32 v40, v45, v41
	v_mul_f32_e32 v44, 0x42800000, v47
	v_mul_f32_e32 v41, 0x42800000, v51
	v_med3_f32 v44, v44, s11, v232
	v_med3_f32 v41, v41, s11, v232
	v_cvt_pk_fp8_f32 v40, v44, v41 op_sel:[0,0,1]
	v_mul_f32_e32 v41, 0x42800000, v55
	v_mul_f32_e32 v44, 0x42800000, v57
	v_med3_f32 v46, v41, s11, v232
	v_med3_f32 v44, v44, s11, v232
	v_mov_b32_e32 v41, v49
	v_cvt_pk_fp8_f32 v41, v46, v44
	s_addc_u32 s5, s0, 0
	v_lshl_add_u64 v[62:63], s[4:5], 0, v[2:3]
	v_mul_f32_e32 v45, 0x42800000, v59
	v_mul_f32_e32 v44, 0x42800000, v61
	v_lshl_add_u64 v[64:65], v[62:63], 0, v[4:5]
	v_med3_f32 v45, v45, s11, v232
	v_med3_f32 v44, v44, s11, v232
	global_store_dwordx2 v[64:65], v[52:53], off
	v_cvt_pk_fp8_f32 v41, v45, v44 op_sel:[0,0,1]
	ds_read2_b32 v[46:47], v43 offset0:16 offset1:24
	ds_read2_b32 v[50:51], v43 offset0:49 offset1:57
	ds_read2_b32 v[52:53], v43 offset0:82 offset1:90
	ds_read2_b32 v[54:55], v43 offset0:115 offset1:123
	v_lshl_add_u64 v[44:45], v[62:63], 0, v[6:7]
	s_mov_b64 s[0:1], 0
	global_store_dwordx2 v[44:45], v[40:41], off
	s_waitcnt lgkmcnt(3)
	v_mul_f32_e32 v40, 0x42800000, v46
	s_waitcnt lgkmcnt(2)
	v_mul_f32_e32 v41, 0x42800000, v50
	s_waitcnt lgkmcnt(1)
	v_mul_f32_e32 v44, 0x42800000, v52
	v_med3_f32 v45, v40, s11, v232
	v_med3_f32 v41, v41, s11, v232
	v_mov_b32_e32 v40, v49
	v_cvt_pk_fp8_f32 v40, v45, v41
	v_med3_f32 v41, v44, s11, v232
	ds_read2_b32 v[44:45], v43 offset0:148 offset1:156
	ds_read2_b32 v[56:57], v43 offset0:181 offset1:189
	ds_read2_b32 v[58:59], v43 offset0:214 offset1:222
	s_waitcnt lgkmcnt(3)
	v_mul_f32_e32 v46, 0x42800000, v54
	v_med3_f32 v46, v46, s11, v232
	ds_read2_b32 v[60:61], v43 offset0:247 offset1:255
	v_cvt_pk_fp8_f32 v40, v41, v46 op_sel:[0,0,1]
	s_waitcnt lgkmcnt(3)
	v_mul_f32_e32 v41, 0x42800000, v44
	s_waitcnt lgkmcnt(2)
	v_mul_f32_e32 v44, 0x42800000, v56
	v_med3_f32 v50, v41, s11, v232
	v_med3_f32 v44, v44, s11, v232
	v_mov_b32_e32 v41, v49
	v_cvt_pk_fp8_f32 v41, v50, v44
	s_waitcnt lgkmcnt(1)
	v_mul_f32_e32 v46, 0x42800000, v58
	s_waitcnt lgkmcnt(0)
	v_mul_f32_e32 v44, 0x42800000, v60
	v_med3_f32 v46, v46, s11, v232
	v_med3_f32 v44, v44, s11, v232
	v_cvt_pk_fp8_f32 v41, v46, v44 op_sel:[0,0,1]
	v_mul_f32_e32 v44, 0x42800000, v47
	v_mul_f32_e32 v46, 0x42800000, v51
	v_med3_f32 v50, v44, s11, v232
	v_med3_f32 v46, v46, s11, v232
	v_mov_b32_e32 v44, v49
	v_cvt_pk_fp8_f32 v44, v50, v46
	v_mul_f32_e32 v47, 0x42800000, v53
	v_mul_f32_e32 v46, 0x42800000, v55
	v_med3_f32 v47, v47, s11, v232
	v_med3_f32 v46, v46, s11, v232
	v_cvt_pk_fp8_f32 v44, v47, v46 op_sel:[0,0,1]
	v_mul_f32_e32 v45, 0x42800000, v45
	v_mul_f32_e32 v46, 0x42800000, v57
	v_med3_f32 v50, v45, s11, v232
	v_med3_f32 v46, v46, s11, v232
	v_mov_b32_e32 v45, v49
	v_cvt_pk_fp8_f32 v45, v50, v46
	v_mul_f32_e32 v47, 0x42800000, v59
	v_mul_f32_e32 v46, 0x42800000, v61
	v_med3_f32 v47, v47, s11, v232
	v_med3_f32 v46, v46, s11, v232
	v_cvt_pk_fp8_f32 v45, v47, v46 op_sel:[0,0,1]
	v_lshl_add_u64 v[46:47], v[62:63], 0, v[8:9]
	global_store_dwordx2 v[46:47], v[40:41], off
	v_lshl_add_u64 v[40:41], v[62:63], 0, v[10:11]
	global_store_dwordx2 v[40:41], v[44:45], off
	s_waitcnt lgkmcnt(0)
.LBB0_23:
	s_andn2_b64 vcc, exec, s[0:1]
	s_cbranch_vccnz .LBB0_25
	s_cmpk_gt_u32 s42, 0x2fff
	s_cselect_b64 s[0:1], -1, 0
	s_and_b64 s[0:1], s[0:1], exec
	s_movk_i32 s0, 0xd000
	s_cselect_b32 s0, s0, 0xfffff000
	s_cselect_b32 s22, 0x80, 0
	s_cselect_b32 s1, s8, s6
	s_cselect_b32 s4, s9, s7
	s_add_i32 s43, s0, s42
	s_lshr_b32 s0, s43, 9
	s_lshl_b32 s44, s43, 5
	s_add_u32 s45, s4, s34
	s_addc_u32 s46, s1, s35
	s_mov_b32 s1, s23
	s_lshl_b64 s[4:5], s[0:1], 22
	s_add_u32 s45, s45, s4
	s_addc_u32 s46, s46, s5
	s_lshl_b32 s4, s43, 6
	s_lshl_b64 s[0:1], s[0:1], 11
	s_and_b32 s4, s4, 0x700
	s_or_b32 s0, s0, s4
	s_or_b64 s[0:1], s[0:1], s[22:23]
	s_and_b32 s4, s44, 0x60
	s_or_b32 s0, s0, s4
	s_lshl_b64 s[4:5], s[0:1], 10
	s_add_u32 s1, s21, s4
	s_addc_u32 s0, s30, s5
	s_lshl_b32 s4, s43, 1
	s_lshl_b32 s5, s43, 7
	s_and_b32 s4, s4, 0x3c0
	s_and_b32 s5, s5, 0xf80
	v_add_u32_e32 v40, s4, v1
	s_add_u32 s44, s45, s5
	s_addc_u32 s45, s46, 0
	v_ashrrev_i32_e32 v41, 31, v40
	v_lshl_add_u64 v[44:45], s[44:45], 0, v[48:49]
	v_lshlrev_b64 v[40:41], 12, v[40:41]
	v_lshl_add_u64 v[40:41], v[44:45], 0, v[40:41]
	s_movk_i32 s5, 0x2000
	v_add_co_u32_e32 v44, vcc, s5, v40
	s_movk_i32 s5, 0x4000
	s_nop 0
	v_addc_co_u32_e32 v45, vcc, 0, v41, vcc
	v_add_co_u32_e32 v46, vcc, s5, v40
	s_movk_i32 s5, 0x6000
	s_nop 0
	v_addc_co_u32_e32 v47, vcc, 0, v41, vcc
	v_add_co_u32_e32 v50, vcc, s5, v40
	s_mov_b32 s5, 0x8000
	s_nop 0
	v_addc_co_u32_e32 v51, vcc, 0, v41, vcc
	v_add_co_u32_e32 v52, vcc, s5, v40
	s_mov_b32 s5, 0xa000
	s_nop 0
	v_addc_co_u32_e32 v53, vcc, 0, v41, vcc
	v_add_co_u32_e32 v54, vcc, s5, v40
	s_mov_b32 s5, 0xc000
	s_nop 0
	v_addc_co_u32_e32 v55, vcc, 0, v41, vcc
	v_add_co_u32_e32 v56, vcc, s5, v40
	s_mov_b32 s5, 0xe000
	s_nop 0
	v_addc_co_u32_e32 v57, vcc, 0, v41, vcc
	v_add_co_u32_e32 v58, vcc, s5, v40
	s_mov_b32 s5, 0x10000
	s_nop 0
	v_addc_co_u32_e32 v59, vcc, 0, v41, vcc
	global_load_dword v48, v[40:41], off sc1 nt
	global_load_dword v62, v[44:45], off sc1 nt
	global_load_dword v63, v[46:47], off sc1 nt
	global_load_dword v64, v[50:51], off sc1 nt
	global_load_dword v65, v[52:53], off sc1 nt
	global_load_dword v66, v[54:55], off sc1 nt
	global_load_dword v67, v[56:57], off sc1 nt
	global_load_dword v68, v[58:59], off sc1 nt
	v_add_co_u32_e32 v44, vcc, s5, v40
	s_mov_b32 s5, 0x12000
	s_nop 0
	v_addc_co_u32_e32 v45, vcc, 0, v41, vcc
	v_add_co_u32_e32 v46, vcc, s5, v40
	s_mov_b32 s5, 0x14000
	s_nop 0
	v_addc_co_u32_e32 v47, vcc, 0, v41, vcc
	v_add_co_u32_e32 v50, vcc, s5, v40
	s_mov_b32 s5, 0x16000
	s_nop 0
	v_addc_co_u32_e32 v51, vcc, 0, v41, vcc
	v_add_co_u32_e32 v52, vcc, s5, v40
	s_mov_b32 s5, 0x18000
	s_nop 0
	v_addc_co_u32_e32 v53, vcc, 0, v41, vcc
	v_add_co_u32_e32 v54, vcc, s5, v40
	s_mov_b32 s5, 0x1a000
	s_nop 0
	v_addc_co_u32_e32 v55, vcc, 0, v41, vcc
	v_add_co_u32_e32 v56, vcc, s5, v40
	s_mov_b32 s5, 0x1c000
	s_nop 0
	v_addc_co_u32_e32 v57, vcc, 0, v41, vcc
	v_add_co_u32_e32 v58, vcc, s5, v40
	s_mov_b32 s5, 0x1e000
	s_nop 0
	v_addc_co_u32_e32 v59, vcc, 0, v41, vcc
	v_add_co_u32_e32 v60, vcc, s5, v40
	s_mov_b32 s5, 0x20000
	s_nop 0
	v_addc_co_u32_e32 v61, vcc, 0, v41, vcc
	global_load_dword v69, v[44:45], off sc1 nt
	global_load_dword v70, v[46:47], off sc1 nt
	global_load_dword v71, v[50:51], off sc1 nt
	global_load_dword v72, v[52:53], off sc1 nt
	global_load_dword v73, v[54:55], off sc1 nt
	global_load_dword v74, v[56:57], off sc1 nt
	global_load_dword v75, v[58:59], off sc1 nt
	global_load_dword v76, v[60:61], off sc1 nt
	v_add_co_u32_e32 v44, vcc, s5, v40
	s_mov_b32 s5, 0x22000
	s_nop 0
	v_addc_co_u32_e32 v45, vcc, 0, v41, vcc
	v_add_co_u32_e32 v46, vcc, s5, v40
	s_mov_b32 s5, 0x24000
	s_nop 0
	v_addc_co_u32_e32 v47, vcc, 0, v41, vcc
	v_add_co_u32_e32 v50, vcc, s5, v40
	s_mov_b32 s5, 0x26000
	s_nop 0
	v_addc_co_u32_e32 v51, vcc, 0, v41, vcc
	v_add_co_u32_e32 v52, vcc, s5, v40
	s_mov_b32 s5, 0x28000
	s_nop 0
	v_addc_co_u32_e32 v53, vcc, 0, v41, vcc
	v_add_co_u32_e32 v54, vcc, s5, v40
	s_mov_b32 s5, 0x2a000
	s_nop 0
	v_addc_co_u32_e32 v55, vcc, 0, v41, vcc
	v_add_co_u32_e32 v56, vcc, s5, v40
	s_mov_b32 s5, 0x2c000
	s_nop 0
	v_addc_co_u32_e32 v57, vcc, 0, v41, vcc
	v_add_co_u32_e32 v58, vcc, s5, v40
	s_mov_b32 s5, 0x2e000
	s_nop 0
	v_addc_co_u32_e32 v59, vcc, 0, v41, vcc
	v_add_co_u32_e32 v60, vcc, s5, v40
	s_mov_b32 s5, 0x30000
	s_nop 0
	v_addc_co_u32_e32 v61, vcc, 0, v41, vcc
	global_load_dword v77, v[44:45], off sc1 nt
	global_load_dword v78, v[46:47], off sc1 nt
	global_load_dword v79, v[50:51], off sc1 nt
	global_load_dword v80, v[52:53], off sc1 nt
	global_load_dword v81, v[54:55], off sc1 nt
	global_load_dword v82, v[56:57], off sc1 nt
	global_load_dword v83, v[58:59], off sc1 nt
	s_nop 0
	global_load_dword v60, v[60:61], off sc1 nt
	v_add_co_u32_e32 v44, vcc, s5, v40
	s_mov_b32 s5, 0x32000
	s_nop 0
	v_addc_co_u32_e32 v45, vcc, 0, v41, vcc
	v_add_co_u32_e32 v46, vcc, s5, v40
	s_mov_b32 s5, 0x34000
	s_nop 0
	v_addc_co_u32_e32 v47, vcc, 0, v41, vcc
	v_add_co_u32_e32 v50, vcc, s5, v40
	s_mov_b32 s5, 0x36000
	s_nop 0
	v_addc_co_u32_e32 v51, vcc, 0, v41, vcc
	v_add_co_u32_e32 v52, vcc, s5, v40
	s_mov_b32 s5, 0x38000
	s_nop 0
	v_addc_co_u32_e32 v53, vcc, 0, v41, vcc
	v_add_co_u32_e32 v54, vcc, s5, v40
	s_mov_b32 s5, 0x3a000
	s_nop 0
	v_addc_co_u32_e32 v55, vcc, 0, v41, vcc
	v_add_co_u32_e32 v56, vcc, s5, v40
	s_mov_b32 s5, 0x3c000
	s_nop 0
	v_addc_co_u32_e32 v57, vcc, 0, v41, vcc
	v_add_co_u32_e32 v58, vcc, s5, v40
	s_mov_b32 s5, 0x3e000
	s_nop 0
	v_addc_co_u32_e32 v59, vcc, 0, v41, vcc
	v_add_co_u32_e32 v40, vcc, s5, v40
	s_lshl_b32 s22, s4, 2
	s_nop 0
	v_addc_co_u32_e32 v41, vcc, 0, v41, vcc
	global_load_dword v44, v[44:45], off sc1 nt
	s_nop 0
	global_load_dword v45, v[46:47], off sc1 nt
	s_nop 0
	global_load_dword v46, v[50:51], off sc1 nt
	global_load_dword v47, v[52:53], off sc1 nt
	s_nop 0
	global_load_dword v50, v[54:55], off sc1 nt
	global_load_dword v51, v[56:57], off sc1 nt
	global_load_dword v52, v[58:59], off sc1 nt
	s_nop 0
	global_load_dword v40, v[40:41], off sc1 nt
	v_add_u32_e32 v41, 0x400, v42
	s_waitcnt vmcnt(30)
	ds_write2_b32 v42, v48, v62 offset1:66
	s_waitcnt vmcnt(28)
	ds_write2_b32 v42, v63, v64 offset0:132 offset1:198
	s_waitcnt vmcnt(26)
	ds_write2_b32 v41, v65, v66 offset0:8 offset1:74
	s_waitcnt vmcnt(24)
	ds_write2_b32 v41, v67, v68 offset0:140 offset1:206
	v_add_u32_e32 v41, 0x800, v42
	s_waitcnt vmcnt(22)
	ds_write2_b32 v41, v69, v70 offset0:16 offset1:82
	s_waitcnt vmcnt(20)
	ds_write2_b32 v41, v71, v72 offset0:148 offset1:214
	v_add_u32_e32 v41, 0xc00, v42
	s_waitcnt vmcnt(18)
	ds_write2_b32 v41, v73, v74 offset0:24 offset1:90
	s_waitcnt vmcnt(16)
	ds_write2_b32 v41, v75, v76 offset0:156 offset1:222
	v_add_u32_e32 v41, 0x1000, v42
	s_waitcnt vmcnt(14)
	ds_write2_b32 v41, v77, v78 offset0:32 offset1:98
	s_waitcnt vmcnt(12)
	ds_write2_b32 v41, v79, v80 offset0:164 offset1:230
	v_add_u32_e32 v41, 0x1400, v42
	s_waitcnt vmcnt(10)
	ds_write2_b32 v41, v81, v82 offset0:40 offset1:106
	s_waitcnt vmcnt(8)
	ds_write2_b32 v41, v83, v60 offset0:172 offset1:238
	v_add_u32_e32 v41, 0x1800, v42
	s_waitcnt vmcnt(6)
	ds_write2_b32 v41, v44, v45 offset0:48 offset1:114
	s_waitcnt vmcnt(4)
	ds_write2_b32 v41, v46, v47 offset0:180 offset1:246
	v_add_u32_e32 v41, 0x1c00, v42
	s_waitcnt vmcnt(2)
	ds_write2_b32 v41, v50, v51 offset0:56 offset1:122
	s_waitcnt vmcnt(0)
	ds_write2_b32 v41, v52, v40 offset0:188 offset1:254
	s_waitcnt lgkmcnt(0)
	v_lshl_add_u64 v[40:41], v[12:13], 0, s[22:23]
	global_load_dwordx4 v[44:47], v[40:41], off
	global_load_dwordx4 v[50:53], v[40:41], off offset:16
	s_mov_b32 s22, 0x42800000
	v_mov_b32_e32 v60, v49
	v_mov_b32_e32 v61, v49
	s_add_u32 s4, s1, s4
	s_addc_u32 s5, s0, 0
	v_lshl_add_u64 v[70:71], s[4:5], 0, v[2:3]
	v_lshl_add_u64 v[72:73], v[70:71], 0, v[4:5]
	s_waitcnt vmcnt(1)
	v_pk_mul_f32 v[40:41], v[46:47], s[22:23] op_sel_hi:[1,0]
	s_waitcnt vmcnt(0)
	v_pk_mul_f32 v[46:47], v[52:53], s[22:23] op_sel_hi:[1,0]
	ds_read2_b32 v[52:53], v43 offset1:8
	ds_read2_b32 v[54:55], v43 offset0:33 offset1:41
	ds_read2_b32 v[56:57], v43 offset0:66 offset1:74
	ds_read2_b32 v[58:59], v43 offset0:99 offset1:107
	v_pk_mul_f32 v[44:45], v[44:45], s[22:23] op_sel_hi:[1,0]
	ds_read2_b32 v[62:63], v43 offset0:132 offset1:140
	ds_read2_b32 v[64:65], v43 offset0:165 offset1:173
	ds_read2_b32 v[66:67], v43 offset0:198 offset1:206
	s_waitcnt lgkmcnt(6)
	v_mul_f32_e32 v48, v44, v52
	s_waitcnt lgkmcnt(5)
	v_mul_f32_e32 v52, v45, v54
	v_med3_f32 v48, v48, s11, v232
	v_med3_f32 v52, v52, s11, v232
	v_cvt_pk_fp8_f32 v60, v48, v52
	s_waitcnt lgkmcnt(4)
	v_mul_f32_e32 v54, v40, v56
	s_waitcnt lgkmcnt(3)
	v_mul_f32_e32 v56, v41, v58
	v_pk_mul_f32 v[50:51], v[50:51], s[22:23] op_sel_hi:[1,0]
	v_med3_f32 v48, v54, s11, v232
	v_med3_f32 v52, v56, s11, v232
	ds_read2_b32 v[68:69], v43 offset0:231 offset1:239
	v_cvt_pk_fp8_f32 v60, v48, v52 op_sel:[0,0,1]
	s_waitcnt lgkmcnt(3)
	v_mul_f32_e32 v48, v50, v62
	s_waitcnt lgkmcnt(2)
	v_mul_f32_e32 v52, v51, v64
	v_med3_f32 v48, v48, s11, v232
	v_med3_f32 v52, v52, s11, v232
	v_cvt_pk_fp8_f32 v61, v48, v52
	s_waitcnt lgkmcnt(1)
	v_mul_f32_e32 v54, v46, v66
	s_waitcnt lgkmcnt(0)
	v_mul_f32_e32 v48, v47, v68
	v_med3_f32 v52, v54, s11, v232
	v_med3_f32 v48, v48, s11, v232
	v_cvt_pk_fp8_f32 v61, v52, v48 op_sel:[0,0,1]
	v_mul_f32_e32 v48, v44, v53
	v_mul_f32_e32 v52, v45, v55
	v_med3_f32 v48, v48, s11, v232
	v_med3_f32 v54, v52, s11, v232
	v_mov_b32_e32 v52, v49
	v_cvt_pk_fp8_f32 v52, v48, v54
	v_mul_f32_e32 v53, v40, v57
	v_mul_f32_e32 v48, v41, v59
	v_med3_f32 v53, v53, s11, v232
	v_med3_f32 v48, v48, s11, v232
	v_cvt_pk_fp8_f32 v52, v53, v48 op_sel:[0,0,1]
	v_mul_f32_e32 v48, v50, v63
	v_mul_f32_e32 v53, v51, v65
	v_med3_f32 v48, v48, s11, v232
	v_med3_f32 v55, v53, s11, v232
	v_mov_b32_e32 v53, v49
	v_cvt_pk_fp8_f32 v53, v48, v55
	v_mul_f32_e32 v54, v46, v67
	v_mul_f32_e32 v48, v47, v69
	v_med3_f32 v54, v54, s11, v232
	v_med3_f32 v48, v48, s11, v232
	global_store_dwordx2 v[72:73], v[60:61], off
	v_cvt_pk_fp8_f32 v53, v54, v48 op_sel:[0,0,1]
	ds_read2_b32 v[56:57], v43 offset0:16 offset1:24
	ds_read2_b32 v[58:59], v43 offset0:49 offset1:57
	ds_read2_b32 v[60:61], v43 offset0:82 offset1:90
	ds_read2_b32 v[62:63], v43 offset0:115 offset1:123
	v_lshl_add_u64 v[54:55], v[70:71], 0, v[6:7]
	s_waitcnt lgkmcnt(3)
	v_mul_f32_e32 v48, v44, v56
	global_store_dwordx2 v[54:55], v[52:53], off
	s_waitcnt lgkmcnt(2)
	v_mul_f32_e32 v52, v45, v58
	v_med3_f32 v48, v48, s11, v232
	v_med3_f32 v54, v52, s11, v232
	v_mov_b32_e32 v52, v49
	v_cvt_pk_fp8_f32 v52, v48, v54
	ds_read2_b32 v[54:55], v43 offset0:148 offset1:156
	ds_read2_b32 v[64:65], v43 offset0:181 offset1:189
	ds_read2_b32 v[66:67], v43 offset0:214 offset1:222
	s_waitcnt lgkmcnt(4)
	v_mul_f32_e32 v53, v40, v60
	s_waitcnt lgkmcnt(3)
	v_mul_f32_e32 v56, v41, v62
	v_med3_f32 v48, v53, s11, v232
	v_med3_f32 v53, v56, s11, v232
	ds_read2_b32 v[68:69], v43 offset0:247 offset1:255
	v_cvt_pk_fp8_f32 v52, v48, v53 op_sel:[0,0,1]
	s_waitcnt lgkmcnt(3)
	v_mul_f32_e32 v48, v50, v54
	s_waitcnt lgkmcnt(2)
	v_mul_f32_e32 v53, v51, v64
	v_med3_f32 v48, v48, s11, v232
	v_med3_f32 v56, v53, s11, v232
	v_mov_b32_e32 v53, v49
	v_cvt_pk_fp8_f32 v53, v48, v56
	s_waitcnt lgkmcnt(1)
	v_mul_f32_e32 v54, v46, v66
	s_waitcnt lgkmcnt(0)
	v_mul_f32_e32 v48, v47, v68
	v_med3_f32 v54, v54, s11, v232
	v_med3_f32 v48, v48, s11, v232
	v_mul_f32_e32 v44, v44, v57
	v_mul_f32_e32 v45, v45, v59
	v_cvt_pk_fp8_f32 v53, v54, v48 op_sel:[0,0,1]
	v_mul_f32_e32 v48, v40, v61
	v_med3_f32 v44, v44, s11, v232
	v_med3_f32 v45, v45, s11, v232
	v_mov_b32_e32 v40, v49
	v_cvt_pk_fp8_f32 v40, v44, v45
	v_mul_f32_e32 v41, v41, v63
	v_med3_f32 v44, v48, s11, v232
	v_med3_f32 v41, v41, s11, v232
	v_cvt_pk_fp8_f32 v40, v44, v41 op_sel:[0,0,1]
	v_mul_f32_e32 v41, v50, v55
	v_mul_f32_e32 v44, v51, v65
	v_mul_f32_e32 v45, v46, v67
	v_med3_f32 v46, v41, s11, v232
	v_med3_f32 v44, v44, s11, v232
	v_mov_b32_e32 v41, v49
	v_cvt_pk_fp8_f32 v41, v46, v44
	v_mul_f32_e32 v44, v47, v69
	v_med3_f32 v45, v45, s11, v232
	v_med3_f32 v44, v44, s11, v232
	v_cvt_pk_fp8_f32 v41, v45, v44 op_sel:[0,0,1]
	v_lshl_add_u64 v[44:45], v[70:71], 0, v[8:9]
	global_store_dwordx2 v[44:45], v[52:53], off
	v_lshl_add_u64 v[44:45], v[70:71], 0, v[10:11]
	global_store_dwordx2 v[44:45], v[40:41], off
	s_waitcnt lgkmcnt(0)

.LBB0_26:
	s_andn2_b64 vcc, exec, s[0:1]
	s_cbranch_vccnz .LBB0_28
	s_and_b32 s5, s39, 0x3e0
	s_lshl_b32 s0, s5, 10
	s_add_u32 s1, s19, s0
	s_addc_u32 s0, s20, 0
	s_and_b32 s4, s41, 0x1fc0
	s_addk_i32 s4, 0xe400
	v_add_u32_e32 v40, s4, v1
	s_lshl_b32 s22, s5, 2
	v_ashrrev_i32_e32 v41, 31, v40
	v_lshl_add_u64 v[44:45], v[14:15], 0, s[22:23]
	v_lshlrev_b64 v[40:41], 12, v[40:41]
	v_lshl_add_u64 v[40:41], v[44:45], 0, v[40:41]
	s_movk_i32 s5, 0x2000
	v_add_co_u32_e32 v44, vcc, s5, v40
	s_movk_i32 s5, 0x4000
	s_nop 0
	v_addc_co_u32_e32 v45, vcc, 0, v41, vcc
	v_add_co_u32_e32 v46, vcc, s5, v40
	s_movk_i32 s5, 0x6000
	s_nop 0
	v_addc_co_u32_e32 v47, vcc, 0, v41, vcc
	v_add_co_u32_e32 v50, vcc, s5, v40
	s_mov_b32 s5, 0x8000
	s_nop 0
	v_addc_co_u32_e32 v51, vcc, 0, v41, vcc
	v_add_co_u32_e32 v52, vcc, s5, v40
	s_mov_b32 s5, 0xa000
	s_nop 0
	v_addc_co_u32_e32 v53, vcc, 0, v41, vcc
	v_add_co_u32_e32 v54, vcc, s5, v40
	s_mov_b32 s5, 0xc000
	s_nop 0
	v_addc_co_u32_e32 v55, vcc, 0, v41, vcc
	v_add_co_u32_e32 v56, vcc, s5, v40
	s_mov_b32 s5, 0xe000
	s_nop 0
	v_addc_co_u32_e32 v57, vcc, 0, v41, vcc
	v_add_co_u32_e32 v58, vcc, s5, v40
	s_mov_b32 s5, 0x10000
	s_nop 0
	v_addc_co_u32_e32 v59, vcc, 0, v41, vcc
	global_load_dword v48, v[40:41], off sc1 nt
	global_load_dword v62, v[44:45], off sc1 nt
	global_load_dword v63, v[46:47], off sc1 nt
	global_load_dword v64, v[50:51], off sc1 nt
	global_load_dword v65, v[52:53], off sc1 nt
	global_load_dword v66, v[54:55], off sc1 nt
	global_load_dword v67, v[56:57], off sc1 nt
	global_load_dword v68, v[58:59], off sc1 nt
	v_add_co_u32_e32 v44, vcc, s5, v40
	s_mov_b32 s5, 0x12000
	s_nop 0
	v_addc_co_u32_e32 v45, vcc, 0, v41, vcc
	v_add_co_u32_e32 v46, vcc, s5, v40
	s_mov_b32 s5, 0x14000
	s_nop 0
	v_addc_co_u32_e32 v47, vcc, 0, v41, vcc
	v_add_co_u32_e32 v50, vcc, s5, v40
	s_mov_b32 s5, 0x16000
	s_nop 0
	v_addc_co_u32_e32 v51, vcc, 0, v41, vcc
	v_add_co_u32_e32 v52, vcc, s5, v40
	s_mov_b32 s5, 0x18000
	s_nop 0
	v_addc_co_u32_e32 v53, vcc, 0, v41, vcc
	v_add_co_u32_e32 v54, vcc, s5, v40
	s_mov_b32 s5, 0x1a000
	s_nop 0
	v_addc_co_u32_e32 v55, vcc, 0, v41, vcc
	v_add_co_u32_e32 v56, vcc, s5, v40
	s_mov_b32 s5, 0x1c000
	s_nop 0
	v_addc_co_u32_e32 v57, vcc, 0, v41, vcc
	v_add_co_u32_e32 v58, vcc, s5, v40
	s_mov_b32 s5, 0x1e000
	s_nop 0
	v_addc_co_u32_e32 v59, vcc, 0, v41, vcc
	v_add_co_u32_e32 v60, vcc, s5, v40
	s_mov_b32 s5, 0x20000
	s_nop 0
	v_addc_co_u32_e32 v61, vcc, 0, v41, vcc
	global_load_dword v69, v[44:45], off sc1 nt
	global_load_dword v70, v[46:47], off sc1 nt
	global_load_dword v71, v[50:51], off sc1 nt
	global_load_dword v72, v[52:53], off sc1 nt
	global_load_dword v73, v[54:55], off sc1 nt
	global_load_dword v74, v[56:57], off sc1 nt
	global_load_dword v75, v[58:59], off sc1 nt
	global_load_dword v76, v[60:61], off sc1 nt
	v_add_co_u32_e32 v44, vcc, s5, v40
	s_mov_b32 s5, 0x22000
	s_nop 0
	v_addc_co_u32_e32 v45, vcc, 0, v41, vcc
	v_add_co_u32_e32 v46, vcc, s5, v40
	s_mov_b32 s5, 0x24000
	s_nop 0
	v_addc_co_u32_e32 v47, vcc, 0, v41, vcc
	v_add_co_u32_e32 v50, vcc, s5, v40
	s_mov_b32 s5, 0x26000
	s_nop 0
	v_addc_co_u32_e32 v51, vcc, 0, v41, vcc
	v_add_co_u32_e32 v52, vcc, s5, v40
	s_mov_b32 s5, 0x28000
	s_nop 0
	v_addc_co_u32_e32 v53, vcc, 0, v41, vcc
	v_add_co_u32_e32 v54, vcc, s5, v40
	s_mov_b32 s5, 0x2a000
	s_nop 0
	v_addc_co_u32_e32 v55, vcc, 0, v41, vcc
	v_add_co_u32_e32 v56, vcc, s5, v40
	s_mov_b32 s5, 0x2c000
	s_nop 0
	v_addc_co_u32_e32 v57, vcc, 0, v41, vcc
	v_add_co_u32_e32 v58, vcc, s5, v40
	s_mov_b32 s5, 0x2e000
	s_nop 0
	v_addc_co_u32_e32 v59, vcc, 0, v41, vcc
	v_add_co_u32_e32 v60, vcc, s5, v40
	s_mov_b32 s5, 0x30000
	s_nop 0
	v_addc_co_u32_e32 v61, vcc, 0, v41, vcc
	global_load_dword v77, v[44:45], off sc1 nt
	global_load_dword v78, v[46:47], off sc1 nt
	global_load_dword v79, v[50:51], off sc1 nt
	global_load_dword v80, v[52:53], off sc1 nt
	global_load_dword v81, v[54:55], off sc1 nt
	global_load_dword v82, v[56:57], off sc1 nt
	global_load_dword v83, v[58:59], off sc1 nt
	s_nop 0
	global_load_dword v60, v[60:61], off sc1 nt
	v_add_co_u32_e32 v44, vcc, s5, v40
	s_mov_b32 s5, 0x32000
	s_nop 0
	v_addc_co_u32_e32 v45, vcc, 0, v41, vcc
	v_add_co_u32_e32 v46, vcc, s5, v40
	s_mov_b32 s5, 0x34000
	s_nop 0
	v_addc_co_u32_e32 v47, vcc, 0, v41, vcc
	v_add_co_u32_e32 v50, vcc, s5, v40
	s_mov_b32 s5, 0x36000
	s_nop 0
	v_addc_co_u32_e32 v51, vcc, 0, v41, vcc
	v_add_co_u32_e32 v52, vcc, s5, v40
	s_mov_b32 s5, 0x38000
	s_nop 0
	v_addc_co_u32_e32 v53, vcc, 0, v41, vcc
	v_add_co_u32_e32 v54, vcc, s5, v40
	s_mov_b32 s5, 0x3a000
	s_nop 0
	v_addc_co_u32_e32 v55, vcc, 0, v41, vcc
	v_add_co_u32_e32 v56, vcc, s5, v40
	s_mov_b32 s5, 0x3c000
	s_nop 0
	v_addc_co_u32_e32 v57, vcc, 0, v41, vcc
	v_add_co_u32_e32 v58, vcc, s5, v40
	s_mov_b32 s5, 0x3e000
	s_nop 0
	v_addc_co_u32_e32 v59, vcc, 0, v41, vcc
	v_add_co_u32_e32 v40, vcc, s5, v40
	s_add_u32 s4, s1, s4
	s_nop 0
	v_addc_co_u32_e32 v41, vcc, 0, v41, vcc
	global_load_dword v44, v[44:45], off sc1 nt
	s_nop 0
	global_load_dword v45, v[46:47], off sc1 nt
	s_nop 0
	global_load_dword v46, v[50:51], off sc1 nt
	global_load_dword v47, v[52:53], off sc1 nt
	s_nop 0
	global_load_dword v50, v[54:55], off sc1 nt
	global_load_dword v51, v[56:57], off sc1 nt
	global_load_dword v52, v[58:59], off sc1 nt
	s_nop 0
	global_load_dword v40, v[40:41], off sc1 nt
	v_add_u32_e32 v41, 0x400, v42
	s_waitcnt vmcnt(30)
	ds_write2_b32 v42, v48, v62 offset1:66
	s_waitcnt vmcnt(28)
	ds_write2_b32 v42, v63, v64 offset0:132 offset1:198
	s_waitcnt vmcnt(26)
	ds_write2_b32 v41, v65, v66 offset0:8 offset1:74
	s_waitcnt vmcnt(24)
	ds_write2_b32 v41, v67, v68 offset0:140 offset1:206
	v_add_u32_e32 v41, 0x800, v42
	s_waitcnt vmcnt(22)
	ds_write2_b32 v41, v69, v70 offset0:16 offset1:82
	s_waitcnt vmcnt(20)
	ds_write2_b32 v41, v71, v72 offset0:148 offset1:214
	v_add_u32_e32 v41, 0xc00, v42
	s_waitcnt vmcnt(18)
	ds_write2_b32 v41, v73, v74 offset0:24 offset1:90
	s_waitcnt vmcnt(16)
	ds_write2_b32 v41, v75, v76 offset0:156 offset1:222
	v_add_u32_e32 v41, 0x1000, v42
	s_waitcnt vmcnt(14)
	ds_write2_b32 v41, v77, v78 offset0:32 offset1:98
	s_waitcnt vmcnt(12)
	ds_write2_b32 v41, v79, v80 offset0:164 offset1:230
	v_add_u32_e32 v41, 0x1400, v42
	s_waitcnt vmcnt(10)
	ds_write2_b32 v41, v81, v82 offset0:40 offset1:106
	s_waitcnt vmcnt(8)
	ds_write2_b32 v41, v83, v60 offset0:172 offset1:238
	v_add_u32_e32 v41, 0x1800, v42
	s_waitcnt vmcnt(6)
	ds_write2_b32 v41, v44, v45 offset0:48 offset1:114
	s_waitcnt vmcnt(4)
	ds_write2_b32 v41, v46, v47 offset0:180 offset1:246
	v_add_u32_e32 v41, 0x1c00, v42
	s_waitcnt vmcnt(2)
	ds_write2_b32 v41, v50, v51 offset0:56 offset1:122
	s_waitcnt vmcnt(0)
	ds_write2_b32 v41, v52, v40 offset0:188 offset1:254
	s_waitcnt lgkmcnt(0)
	ds_read2_b32 v[40:41], v43 offset1:8
	ds_read2_b32 v[44:45], v43 offset0:33 offset1:41
	ds_read2_b32 v[46:47], v43 offset0:66 offset1:74
	ds_read2_b32 v[50:51], v43 offset0:99 offset1:107
	v_mov_b32_e32 v52, v49
	s_waitcnt lgkmcnt(3)
	v_mul_f32_e32 v40, 0x42800000, v40
	s_waitcnt lgkmcnt(2)
	v_mul_f32_e32 v44, 0x42800000, v44
	v_med3_f32 v40, v40, s11, v232
	v_med3_f32 v44, v44, s11, v232
	v_cvt_pk_fp8_f32 v52, v40, v44
	ds_read2_b32 v[54:55], v43 offset0:132 offset1:140
	ds_read2_b32 v[56:57], v43 offset0:165 offset1:173
	ds_read2_b32 v[58:59], v43 offset0:198 offset1:206
	s_waitcnt lgkmcnt(4)
	v_mul_f32_e32 v46, 0x42800000, v46
	s_waitcnt lgkmcnt(3)
	v_mul_f32_e32 v48, 0x42800000, v50
	v_med3_f32 v40, v46, s11, v232
	v_med3_f32 v44, v48, s11, v232
	ds_read2_b32 v[60:61], v43 offset0:231 offset1:239
	v_cvt_pk_fp8_f32 v52, v40, v44 op_sel:[0,0,1]
	s_waitcnt lgkmcnt(3)
	v_mul_f32_e32 v40, 0x42800000, v54
	s_waitcnt lgkmcnt(2)
	v_mul_f32_e32 v44, 0x42800000, v56
	v_med3_f32 v40, v40, s11, v232
	v_med3_f32 v44, v44, s11, v232
	v_mov_b32_e32 v53, v49
	v_cvt_pk_fp8_f32 v53, v40, v44
	s_waitcnt lgkmcnt(1)
	v_mul_f32_e32 v46, 0x42800000, v58
	s_waitcnt lgkmcnt(0)
	v_mul_f32_e32 v40, 0x42800000, v60
	v_med3_f32 v44, v46, s11, v232
	v_med3_f32 v40, v40, s11, v232
	v_cvt_pk_fp8_f32 v53, v44, v40 op_sel:[0,0,1]
	v_mul_f32_e32 v40, 0x42800000, v41
	v_mul_f32_e32 v41, 0x42800000, v45
	v_med3_f32 v45, v40, s11, v232
	v_med3_f32 v41, v41, s11, v232
	v_mov_b32_e32 v40, v49
	v_cvt_pk_fp8_f32 v40, v45, v41
	v_mul_f32_e32 v44, 0x42800000, v47
	v_mul_f32_e32 v41, 0x42800000, v51
	v_med3_f32 v44, v44, s11, v232
	v_med3_f32 v41, v41, s11, v232
	v_cvt_pk_fp8_f32 v40, v44, v41 op_sel:[0,0,1]
	v_mul_f32_e32 v41, 0x42800000, v55
	v_mul_f32_e32 v44, 0x42800000, v57
	v_med3_f32 v46, v41, s11, v232
	v_med3_f32 v44, v44, s11, v232
	v_mov_b32_e32 v41, v49
	v_cvt_pk_fp8_f32 v41, v46, v44
	s_addc_u32 s5, s0, 0
	v_lshl_add_u64 v[62:63], s[4:5], 0, v[2:3]
	v_mul_f32_e32 v45, 0x42800000, v59
	v_mul_f32_e32 v44, 0x42800000, v61
	v_lshl_add_u64 v[64:65], v[62:63], 0, v[4:5]
	v_med3_f32 v45, v45, s11, v232
	v_med3_f32 v44, v44, s11, v232
	global_store_dwordx2 v[64:65], v[52:53], off
	v_cvt_pk_fp8_f32 v41, v45, v44 op_sel:[0,0,1]
	ds_read2_b32 v[46:47], v43 offset0:16 offset1:24
	ds_read2_b32 v[50:51], v43 offset0:49 offset1:57
	ds_read2_b32 v[52:53], v43 offset0:82 offset1:90
	ds_read2_b32 v[54:55], v43 offset0:115 offset1:123
	v_lshl_add_u64 v[44:45], v[62:63], 0, v[6:7]
	global_store_dwordx2 v[44:45], v[40:41], off
	s_waitcnt lgkmcnt(3)
	v_mul_f32_e32 v40, 0x42800000, v46
	s_waitcnt lgkmcnt(2)
	v_mul_f32_e32 v41, 0x42800000, v50
	s_waitcnt lgkmcnt(1)
	v_mul_f32_e32 v44, 0x42800000, v52
	v_med3_f32 v45, v40, s11, v232
	v_med3_f32 v41, v41, s11, v232
	v_mov_b32_e32 v40, v49
	v_cvt_pk_fp8_f32 v40, v45, v41
	v_med3_f32 v41, v44, s11, v232
	ds_read2_b32 v[44:45], v43 offset0:148 offset1:156
	ds_read2_b32 v[56:57], v43 offset0:181 offset1:189
	ds_read2_b32 v[58:59], v43 offset0:214 offset1:222
	s_waitcnt lgkmcnt(3)
	v_mul_f32_e32 v46, 0x42800000, v54
	v_med3_f32 v46, v46, s11, v232
	ds_read2_b32 v[60:61], v43 offset0:247 offset1:255
	v_cvt_pk_fp8_f32 v40, v41, v46 op_sel:[0,0,1]
	s_waitcnt lgkmcnt(3)
	v_mul_f32_e32 v41, 0x42800000, v44
	s_waitcnt lgkmcnt(2)
	v_mul_f32_e32 v44, 0x42800000, v56
	v_med3_f32 v48, v41, s11, v232
	v_med3_f32 v44, v44, s11, v232
	v_mov_b32_e32 v41, v49
	v_cvt_pk_fp8_f32 v41, v48, v44
	s_waitcnt lgkmcnt(1)
	v_mul_f32_e32 v46, 0x42800000, v58
	s_waitcnt lgkmcnt(0)
	v_mul_f32_e32 v44, 0x42800000, v60
	v_med3_f32 v46, v46, s11, v232
	v_med3_f32 v44, v44, s11, v232
	v_cvt_pk_fp8_f32 v41, v46, v44 op_sel:[0,0,1]
	v_mul_f32_e32 v44, 0x42800000, v47
	v_mul_f32_e32 v46, 0x42800000, v51
	v_med3_f32 v48, v44, s11, v232
	v_med3_f32 v46, v46, s11, v232
	v_mov_b32_e32 v44, v49
	v_cvt_pk_fp8_f32 v44, v48, v46
	v_mul_f32_e32 v47, 0x42800000, v53
	v_mul_f32_e32 v46, 0x42800000, v55
	v_med3_f32 v47, v47, s11, v232
	v_med3_f32 v46, v46, s11, v232
	v_cvt_pk_fp8_f32 v44, v47, v46 op_sel:[0,0,1]
	v_mul_f32_e32 v45, 0x42800000, v45
	v_mul_f32_e32 v46, 0x42800000, v57
	v_med3_f32 v48, v45, s11, v232
	v_med3_f32 v46, v46, s11, v232
	v_mov_b32_e32 v45, v49
	v_cvt_pk_fp8_f32 v45, v48, v46
	v_mul_f32_e32 v47, 0x42800000, v59
	v_mul_f32_e32 v46, 0x42800000, v61
	v_med3_f32 v47, v47, s11, v232
	v_med3_f32 v46, v46, s11, v232
	v_cvt_pk_fp8_f32 v45, v47, v46 op_sel:[0,0,1]
	v_lshl_add_u64 v[46:47], v[62:63], 0, v[8:9]
	global_store_dwordx2 v[46:47], v[40:41], off
	v_lshl_add_u64 v[40:41], v[62:63], 0, v[10:11]
	global_store_dwordx2 v[40:41], v[44:45], off
	s_waitcnt lgkmcnt(0)

.LBB0_29:
	s_andn2_b64 vcc, exec, s[0:1]
	s_cbranch_vccnz .LBB0_31
	s_and_b32 s1, s39, 0x3e0
	s_lshl_b32 s0, s1, 11
	s_add_u32 s4, s16, s0
	s_addc_u32 s5, s18, 0
	s_and_b32 s0, s41, 0x1fc0
	s_addk_i32 s0, 0xe800
	v_add_u32_e32 v40, s0, v1
	s_lshl_b32 s22, s1, 2
	v_ashrrev_i32_e32 v41, 31, v40
	v_lshl_add_u64 v[44:45], v[16:17], 0, s[22:23]
	v_lshlrev_b64 v[40:41], 12, v[40:41]
	v_lshl_add_u64 v[40:41], v[44:45], 0, v[40:41]
	s_movk_i32 s1, 0x2000
	v_add_co_u32_e32 v44, vcc, s1, v40
	s_movk_i32 s1, 0x4000
	s_nop 0
	v_addc_co_u32_e32 v45, vcc, 0, v41, vcc
	v_add_co_u32_e32 v46, vcc, s1, v40
	s_movk_i32 s1, 0x6000
	s_nop 0
	v_addc_co_u32_e32 v47, vcc, 0, v41, vcc
	v_add_co_u32_e32 v50, vcc, s1, v40
	s_mov_b32 s1, 0x8000
	s_nop 0
	v_addc_co_u32_e32 v51, vcc, 0, v41, vcc
	v_add_co_u32_e32 v52, vcc, s1, v40
	s_mov_b32 s1, 0xa000
	s_nop 0
	v_addc_co_u32_e32 v53, vcc, 0, v41, vcc
	v_add_co_u32_e32 v54, vcc, s1, v40
	s_mov_b32 s1, 0xc000
	s_nop 0
	v_addc_co_u32_e32 v55, vcc, 0, v41, vcc
	v_add_co_u32_e32 v56, vcc, s1, v40
	s_mov_b32 s1, 0xe000
	s_nop 0
	v_addc_co_u32_e32 v57, vcc, 0, v41, vcc
	v_add_co_u32_e32 v58, vcc, s1, v40
	s_mov_b32 s1, 0x10000
	s_nop 0
	v_addc_co_u32_e32 v59, vcc, 0, v41, vcc
	global_load_dword v48, v[40:41], off sc1 nt
	global_load_dword v62, v[44:45], off sc1 nt
	global_load_dword v63, v[46:47], off sc1 nt
	global_load_dword v64, v[50:51], off sc1 nt
	global_load_dword v65, v[52:53], off sc1 nt
	global_load_dword v66, v[54:55], off sc1 nt
	global_load_dword v67, v[56:57], off sc1 nt
	global_load_dword v68, v[58:59], off sc1 nt
	v_add_co_u32_e32 v44, vcc, s1, v40
	s_mov_b32 s1, 0x12000
	s_nop 0
	v_addc_co_u32_e32 v45, vcc, 0, v41, vcc
	v_add_co_u32_e32 v46, vcc, s1, v40
	s_mov_b32 s1, 0x14000
	s_nop 0
	v_addc_co_u32_e32 v47, vcc, 0, v41, vcc
	v_add_co_u32_e32 v50, vcc, s1, v40
	s_mov_b32 s1, 0x16000
	s_nop 0
	v_addc_co_u32_e32 v51, vcc, 0, v41, vcc
	v_add_co_u32_e32 v52, vcc, s1, v40
	s_mov_b32 s1, 0x18000
	s_nop 0
	v_addc_co_u32_e32 v53, vcc, 0, v41, vcc
	v_add_co_u32_e32 v54, vcc, s1, v40
	s_mov_b32 s1, 0x1a000
	s_nop 0
	v_addc_co_u32_e32 v55, vcc, 0, v41, vcc
	v_add_co_u32_e32 v56, vcc, s1, v40
	s_mov_b32 s1, 0x1c000
	s_nop 0
	v_addc_co_u32_e32 v57, vcc, 0, v41, vcc
	v_add_co_u32_e32 v58, vcc, s1, v40
	s_mov_b32 s1, 0x1e000
	s_nop 0
	v_addc_co_u32_e32 v59, vcc, 0, v41, vcc
	v_add_co_u32_e32 v60, vcc, s1, v40
	s_mov_b32 s1, 0x20000
	s_nop 0
	v_addc_co_u32_e32 v61, vcc, 0, v41, vcc
	global_load_dword v69, v[44:45], off sc1 nt
	global_load_dword v70, v[46:47], off sc1 nt
	global_load_dword v71, v[50:51], off sc1 nt
	global_load_dword v72, v[52:53], off sc1 nt
	global_load_dword v73, v[54:55], off sc1 nt
	global_load_dword v74, v[56:57], off sc1 nt
	global_load_dword v75, v[58:59], off sc1 nt
	global_load_dword v76, v[60:61], off sc1 nt
	v_add_co_u32_e32 v44, vcc, s1, v40
	s_mov_b32 s1, 0x22000
	s_nop 0
	v_addc_co_u32_e32 v45, vcc, 0, v41, vcc
	v_add_co_u32_e32 v46, vcc, s1, v40
	s_mov_b32 s1, 0x24000
	s_nop 0
	v_addc_co_u32_e32 v47, vcc, 0, v41, vcc
	v_add_co_u32_e32 v50, vcc, s1, v40
	s_mov_b32 s1, 0x26000
	s_nop 0
	v_addc_co_u32_e32 v51, vcc, 0, v41, vcc
	v_add_co_u32_e32 v52, vcc, s1, v40
	s_mov_b32 s1, 0x28000
	s_nop 0
	v_addc_co_u32_e32 v53, vcc, 0, v41, vcc
	v_add_co_u32_e32 v54, vcc, s1, v40
	s_mov_b32 s1, 0x2a000
	s_nop 0
	v_addc_co_u32_e32 v55, vcc, 0, v41, vcc
	v_add_co_u32_e32 v56, vcc, s1, v40
	s_mov_b32 s1, 0x2c000
	s_nop 0
	v_addc_co_u32_e32 v57, vcc, 0, v41, vcc
	v_add_co_u32_e32 v58, vcc, s1, v40
	s_mov_b32 s1, 0x2e000
	s_nop 0
	v_addc_co_u32_e32 v59, vcc, 0, v41, vcc
	v_add_co_u32_e32 v60, vcc, s1, v40
	s_mov_b32 s1, 0x30000
	s_nop 0
	v_addc_co_u32_e32 v61, vcc, 0, v41, vcc
	global_load_dword v77, v[44:45], off sc1 nt
	global_load_dword v78, v[46:47], off sc1 nt
	global_load_dword v79, v[50:51], off sc1 nt
	global_load_dword v80, v[52:53], off sc1 nt
	global_load_dword v81, v[54:55], off sc1 nt
	global_load_dword v82, v[56:57], off sc1 nt
	global_load_dword v83, v[58:59], off sc1 nt
	s_nop 0
	global_load_dword v60, v[60:61], off sc1 nt
	v_add_co_u32_e32 v44, vcc, s1, v40
	s_mov_b32 s1, 0x32000
	s_nop 0
	v_addc_co_u32_e32 v45, vcc, 0, v41, vcc
	v_add_co_u32_e32 v46, vcc, s1, v40
	s_mov_b32 s1, 0x34000
	s_nop 0
	v_addc_co_u32_e32 v47, vcc, 0, v41, vcc
	v_add_co_u32_e32 v50, vcc, s1, v40
	s_mov_b32 s1, 0x36000
	s_nop 0
	v_addc_co_u32_e32 v51, vcc, 0, v41, vcc
	v_add_co_u32_e32 v52, vcc, s1, v40
	s_mov_b32 s1, 0x38000
	s_nop 0
	v_addc_co_u32_e32 v53, vcc, 0, v41, vcc
	v_add_co_u32_e32 v54, vcc, s1, v40
	s_mov_b32 s1, 0x3a000
	s_nop 0
	v_addc_co_u32_e32 v55, vcc, 0, v41, vcc
	v_add_co_u32_e32 v56, vcc, s1, v40
	s_mov_b32 s1, 0x3c000
	s_nop 0
	v_addc_co_u32_e32 v57, vcc, 0, v41, vcc
	v_add_co_u32_e32 v58, vcc, s1, v40
	s_mov_b32 s1, 0x3e000
	s_nop 0
	v_addc_co_u32_e32 v59, vcc, 0, v41, vcc
	v_add_co_u32_e32 v40, vcc, s1, v40
	s_mov_b32 s1, s23
	s_nop 0
	v_addc_co_u32_e32 v41, vcc, 0, v41, vcc
	global_load_dword v44, v[44:45], off sc1 nt
	s_nop 0
	global_load_dword v45, v[46:47], off sc1 nt
	s_nop 0
	global_load_dword v46, v[50:51], off sc1 nt
	global_load_dword v47, v[52:53], off sc1 nt
	s_nop 0
	global_load_dword v50, v[54:55], off sc1 nt
	global_load_dword v51, v[56:57], off sc1 nt
	global_load_dword v52, v[58:59], off sc1 nt
	s_nop 0
	global_load_dword v40, v[40:41], off sc1 nt
	v_add_u32_e32 v41, 0x400, v42
	s_waitcnt vmcnt(30)
	ds_write2_b32 v42, v48, v62 offset1:66
	s_waitcnt vmcnt(28)
	ds_write2_b32 v42, v63, v64 offset0:132 offset1:198
	s_waitcnt vmcnt(26)
	ds_write2_b32 v41, v65, v66 offset0:8 offset1:74
	s_waitcnt vmcnt(24)
	ds_write2_b32 v41, v67, v68 offset0:140 offset1:206
	v_add_u32_e32 v41, 0x800, v42
	s_waitcnt vmcnt(22)
	ds_write2_b32 v41, v69, v70 offset0:16 offset1:82
	s_waitcnt vmcnt(20)
	ds_write2_b32 v41, v71, v72 offset0:148 offset1:214
	v_add_u32_e32 v41, 0xc00, v42
	s_waitcnt vmcnt(18)
	ds_write2_b32 v41, v73, v74 offset0:24 offset1:90
	s_waitcnt vmcnt(16)
	ds_write2_b32 v41, v75, v76 offset0:156 offset1:222
	v_add_u32_e32 v41, 0x1000, v42
	s_waitcnt vmcnt(14)
	ds_write2_b32 v41, v77, v78 offset0:32 offset1:98
	s_waitcnt vmcnt(12)
	ds_write2_b32 v41, v79, v80 offset0:164 offset1:230
	v_add_u32_e32 v41, 0x1400, v42
	s_waitcnt vmcnt(10)
	ds_write2_b32 v41, v81, v82 offset0:40 offset1:106
	s_waitcnt vmcnt(8)
	ds_write2_b32 v41, v83, v60 offset0:172 offset1:238
	v_add_u32_e32 v41, 0x1800, v42
	s_waitcnt vmcnt(6)
	ds_write2_b32 v41, v44, v45 offset0:48 offset1:114
	s_waitcnt vmcnt(4)
	ds_write2_b32 v41, v46, v47 offset0:180 offset1:246
	v_add_u32_e32 v41, 0x1c00, v42
	s_waitcnt vmcnt(2)
	ds_write2_b32 v41, v50, v51 offset0:56 offset1:122
	s_waitcnt vmcnt(0)
	ds_write2_b32 v41, v52, v40 offset0:188 offset1:254
	s_waitcnt lgkmcnt(0)
	ds_read2_b32 v[40:41], v43 offset0:33 offset1:41
	ds_read2_b32 v[50:51], v43 offset1:8
	ds_read2_b32 v[52:53], v43 offset0:66 offset1:74
	ds_read2_b32 v[54:55], v43 offset0:99 offset1:107
	ds_read2_b32 v[56:57], v43 offset0:132 offset1:140
	ds_read2_b32 v[58:59], v43 offset0:165 offset1:173
	ds_read2_b32 v[60:61], v43 offset0:198 offset1:206
	ds_read2_b32 v[62:63], v43 offset0:231 offset1:239
	s_lshl_b64 s[0:1], s[0:1], 1
	s_add_u32 s0, s4, s0
	s_addc_u32 s1, s5, s1
	v_lshlrev_b32_e32 v48, 1, v2
	v_lshl_add_u64 v[64:65], s[0:1], 0, v[48:49]
	s_waitcnt lgkmcnt(6)
	v_cvt_pk_bf16_f32 v44, v50, v40
	s_waitcnt lgkmcnt(4)
	v_cvt_pk_bf16_f32 v45, v52, v54
	s_waitcnt lgkmcnt(2)
	v_cvt_pk_bf16_f32 v46, v56, v58
	s_waitcnt lgkmcnt(0)
	v_cvt_pk_bf16_f32 v47, v60, v62
	v_lshl_add_u64 v[66:67], v[64:65], 0, v[18:19]
	global_store_dwordx4 v[66:67], v[44:47], off
	s_nop 1
	v_cvt_pk_bf16_f32 v44, v51, v41
	v_cvt_pk_bf16_f32 v45, v53, v55
	v_cvt_pk_bf16_f32 v46, v57, v59
	v_cvt_pk_bf16_f32 v47, v61, v63
	ds_read2_b32 v[50:51], v43 offset0:49 offset1:57
	ds_read2_b32 v[52:53], v43 offset0:16 offset1:24
	ds_read2_b32 v[54:55], v43 offset0:82 offset1:90
	ds_read2_b32 v[56:57], v43 offset0:115 offset1:123
	ds_read2_b32 v[58:59], v43 offset0:148 offset1:156
	ds_read2_b32 v[60:61], v43 offset0:181 offset1:189
	ds_read2_b32 v[62:63], v43 offset0:214 offset1:222
	ds_read2_b32 v[66:67], v43 offset0:247 offset1:255
	v_lshl_add_u64 v[40:41], v[64:65], 0, v[20:21]
	global_store_dwordx4 v[40:41], v[44:47], off
	v_lshl_add_u64 v[40:41], v[64:65], 0, v[22:23]
	s_waitcnt lgkmcnt(6)
	v_cvt_pk_bf16_f32 v44, v52, v50
	s_waitcnt lgkmcnt(4)
	v_cvt_pk_bf16_f32 v45, v54, v56
	s_waitcnt lgkmcnt(2)
	v_cvt_pk_bf16_f32 v46, v58, v60
	s_waitcnt lgkmcnt(0)
	v_cvt_pk_bf16_f32 v47, v62, v66
	global_store_dwordx4 v[40:41], v[44:47], off
	v_lshl_add_u64 v[40:41], v[64:65], 0, v[24:25]
	s_nop 0
	v_cvt_pk_bf16_f32 v44, v53, v51
	v_cvt_pk_bf16_f32 v45, v55, v57
	v_cvt_pk_bf16_f32 v46, v59, v61
	v_cvt_pk_bf16_f32 v47, v63, v67
	global_store_dwordx4 v[40:41], v[44:47], off
	s_waitcnt lgkmcnt(0)

.LBB0_32:
	s_andn2_b64 vcc, exec, s[0:1]
	s_cbranch_vccnz .LBB0_34
	s_and_b32 s1, s39, 0x3e0
	s_lshl_b32 s0, s1, 9
	s_add_u32 s4, s13, s0
	s_addc_u32 s5, s14, 0
	s_and_b32 s0, s41, 0x1fc0
	s_addk_i32 s0, 0xe900
	v_add_u32_e32 v40, s0, v1
	s_lshl_b32 s22, s1, 2
	v_ashrrev_i32_e32 v41, 31, v40
	v_lshl_add_u64 v[44:45], v[26:27], 0, s[22:23]
	v_lshlrev_b64 v[40:41], 12, v[40:41]
	v_lshl_add_u64 v[40:41], v[44:45], 0, v[40:41]
	s_movk_i32 s1, 0x2000
	v_add_co_u32_e32 v44, vcc, s1, v40
	s_movk_i32 s1, 0x4000
	s_nop 0
	v_addc_co_u32_e32 v45, vcc, 0, v41, vcc
	v_add_co_u32_e32 v46, vcc, s1, v40
	s_movk_i32 s1, 0x6000
	s_nop 0
	v_addc_co_u32_e32 v47, vcc, 0, v41, vcc
	v_add_co_u32_e32 v50, vcc, s1, v40
	s_mov_b32 s1, 0x8000
	s_nop 0
	v_addc_co_u32_e32 v51, vcc, 0, v41, vcc
	v_add_co_u32_e32 v52, vcc, s1, v40
	s_mov_b32 s1, 0xa000
	s_nop 0
	v_addc_co_u32_e32 v53, vcc, 0, v41, vcc
	v_add_co_u32_e32 v54, vcc, s1, v40
	s_mov_b32 s1, 0xc000
	s_nop 0
	v_addc_co_u32_e32 v55, vcc, 0, v41, vcc
	v_add_co_u32_e32 v56, vcc, s1, v40
	s_mov_b32 s1, 0xe000
	s_nop 0
	v_addc_co_u32_e32 v57, vcc, 0, v41, vcc
	v_add_co_u32_e32 v58, vcc, s1, v40
	s_mov_b32 s1, 0x10000
	s_nop 0
	v_addc_co_u32_e32 v59, vcc, 0, v41, vcc
	global_load_dword v48, v[40:41], off sc1 nt
	global_load_dword v62, v[44:45], off sc1 nt
	global_load_dword v63, v[46:47], off sc1 nt
	global_load_dword v64, v[50:51], off sc1 nt
	global_load_dword v65, v[52:53], off sc1 nt
	global_load_dword v66, v[54:55], off sc1 nt
	global_load_dword v67, v[56:57], off sc1 nt
	global_load_dword v68, v[58:59], off sc1 nt
	v_add_co_u32_e32 v44, vcc, s1, v40
	s_mov_b32 s1, 0x12000
	s_nop 0
	v_addc_co_u32_e32 v45, vcc, 0, v41, vcc
	v_add_co_u32_e32 v46, vcc, s1, v40
	s_mov_b32 s1, 0x14000
	s_nop 0
	v_addc_co_u32_e32 v47, vcc, 0, v41, vcc
	v_add_co_u32_e32 v50, vcc, s1, v40
	s_mov_b32 s1, 0x16000
	s_nop 0
	v_addc_co_u32_e32 v51, vcc, 0, v41, vcc
	v_add_co_u32_e32 v52, vcc, s1, v40
	s_mov_b32 s1, 0x18000
	s_nop 0
	v_addc_co_u32_e32 v53, vcc, 0, v41, vcc
	v_add_co_u32_e32 v54, vcc, s1, v40
	s_mov_b32 s1, 0x1a000
	s_nop 0
	v_addc_co_u32_e32 v55, vcc, 0, v41, vcc
	v_add_co_u32_e32 v56, vcc, s1, v40
	s_mov_b32 s1, 0x1c000
	s_nop 0
	v_addc_co_u32_e32 v57, vcc, 0, v41, vcc
	v_add_co_u32_e32 v58, vcc, s1, v40
	s_mov_b32 s1, 0x1e000
	s_nop 0
	v_addc_co_u32_e32 v59, vcc, 0, v41, vcc
	v_add_co_u32_e32 v60, vcc, s1, v40
	s_mov_b32 s1, 0x20000
	s_nop 0
	v_addc_co_u32_e32 v61, vcc, 0, v41, vcc
	global_load_dword v69, v[44:45], off sc1 nt
	global_load_dword v70, v[46:47], off sc1 nt
	global_load_dword v71, v[50:51], off sc1 nt
	global_load_dword v72, v[52:53], off sc1 nt
	global_load_dword v73, v[54:55], off sc1 nt
	global_load_dword v74, v[56:57], off sc1 nt
	global_load_dword v75, v[58:59], off sc1 nt
	global_load_dword v76, v[60:61], off sc1 nt
	v_add_co_u32_e32 v44, vcc, s1, v40
	s_mov_b32 s1, 0x22000
	s_nop 0
	v_addc_co_u32_e32 v45, vcc, 0, v41, vcc
	v_add_co_u32_e32 v46, vcc, s1, v40
	s_mov_b32 s1, 0x24000
	s_nop 0
	v_addc_co_u32_e32 v47, vcc, 0, v41, vcc
	v_add_co_u32_e32 v50, vcc, s1, v40
	s_mov_b32 s1, 0x26000
	s_nop 0
	v_addc_co_u32_e32 v51, vcc, 0, v41, vcc
	v_add_co_u32_e32 v52, vcc, s1, v40
	s_mov_b32 s1, 0x28000
	s_nop 0
	v_addc_co_u32_e32 v53, vcc, 0, v41, vcc
	v_add_co_u32_e32 v54, vcc, s1, v40
	s_mov_b32 s1, 0x2a000
	s_nop 0
	v_addc_co_u32_e32 v55, vcc, 0, v41, vcc
	v_add_co_u32_e32 v56, vcc, s1, v40
	s_mov_b32 s1, 0x2c000
	s_nop 0
	v_addc_co_u32_e32 v57, vcc, 0, v41, vcc
	v_add_co_u32_e32 v58, vcc, s1, v40
	s_mov_b32 s1, 0x2e000
	s_nop 0
	v_addc_co_u32_e32 v59, vcc, 0, v41, vcc
	v_add_co_u32_e32 v60, vcc, s1, v40
	s_mov_b32 s1, 0x30000
	s_nop 0
	v_addc_co_u32_e32 v61, vcc, 0, v41, vcc
	global_load_dword v77, v[44:45], off sc1 nt
	global_load_dword v78, v[46:47], off sc1 nt
	global_load_dword v79, v[50:51], off sc1 nt
	global_load_dword v80, v[52:53], off sc1 nt
	global_load_dword v81, v[54:55], off sc1 nt
	global_load_dword v82, v[56:57], off sc1 nt
	global_load_dword v83, v[58:59], off sc1 nt
	s_nop 0
	global_load_dword v60, v[60:61], off sc1 nt
	v_add_co_u32_e32 v44, vcc, s1, v40
	s_mov_b32 s1, 0x32000
	s_nop 0
	v_addc_co_u32_e32 v45, vcc, 0, v41, vcc
	v_add_co_u32_e32 v46, vcc, s1, v40
	s_mov_b32 s1, 0x34000
	s_nop 0
	v_addc_co_u32_e32 v47, vcc, 0, v41, vcc
	v_add_co_u32_e32 v50, vcc, s1, v40
	s_mov_b32 s1, 0x36000
	s_nop 0
	v_addc_co_u32_e32 v51, vcc, 0, v41, vcc
	v_add_co_u32_e32 v52, vcc, s1, v40
	s_mov_b32 s1, 0x38000
	s_nop 0
	v_addc_co_u32_e32 v53, vcc, 0, v41, vcc
	v_add_co_u32_e32 v54, vcc, s1, v40
	s_mov_b32 s1, 0x3a000
	s_nop 0
	v_addc_co_u32_e32 v55, vcc, 0, v41, vcc
	v_add_co_u32_e32 v56, vcc, s1, v40
	s_mov_b32 s1, 0x3c000
	s_nop 0
	v_addc_co_u32_e32 v57, vcc, 0, v41, vcc
	v_add_co_u32_e32 v58, vcc, s1, v40
	s_mov_b32 s1, 0x3e000
	s_nop 0
	v_addc_co_u32_e32 v59, vcc, 0, v41, vcc
	v_add_co_u32_e32 v40, vcc, s1, v40
	s_mov_b32 s1, s23
	s_nop 0
	v_addc_co_u32_e32 v41, vcc, 0, v41, vcc
	global_load_dword v44, v[44:45], off sc1 nt
	s_nop 0
	global_load_dword v45, v[46:47], off sc1 nt
	s_nop 0
	global_load_dword v46, v[50:51], off sc1 nt
	global_load_dword v47, v[52:53], off sc1 nt
	s_nop 0
	global_load_dword v50, v[54:55], off sc1 nt
	global_load_dword v51, v[56:57], off sc1 nt
	global_load_dword v52, v[58:59], off sc1 nt
	s_nop 0
	global_load_dword v40, v[40:41], off sc1 nt
	v_add_u32_e32 v41, 0x400, v42
	s_waitcnt vmcnt(30)
	ds_write2_b32 v42, v48, v62 offset1:66
	s_waitcnt vmcnt(28)
	ds_write2_b32 v42, v63, v64 offset0:132 offset1:198
	s_waitcnt vmcnt(26)
	ds_write2_b32 v41, v65, v66 offset0:8 offset1:74
	s_waitcnt vmcnt(24)
	ds_write2_b32 v41, v67, v68 offset0:140 offset1:206
	v_add_u32_e32 v41, 0x800, v42
	s_waitcnt vmcnt(22)
	ds_write2_b32 v41, v69, v70 offset0:16 offset1:82
	s_waitcnt vmcnt(20)
	ds_write2_b32 v41, v71, v72 offset0:148 offset1:214
	v_add_u32_e32 v41, 0xc00, v42
	s_waitcnt vmcnt(18)
	ds_write2_b32 v41, v73, v74 offset0:24 offset1:90
	s_waitcnt vmcnt(16)
	ds_write2_b32 v41, v75, v76 offset0:156 offset1:222
	v_add_u32_e32 v41, 0x1000, v42
	s_waitcnt vmcnt(14)
	ds_write2_b32 v41, v77, v78 offset0:32 offset1:98
	s_waitcnt vmcnt(12)
	ds_write2_b32 v41, v79, v80 offset0:164 offset1:230
	v_add_u32_e32 v41, 0x1400, v42
	s_waitcnt vmcnt(10)
	ds_write2_b32 v41, v81, v82 offset0:40 offset1:106
	s_waitcnt vmcnt(8)
	ds_write2_b32 v41, v83, v60 offset0:172 offset1:238
	v_add_u32_e32 v41, 0x1800, v42
	s_waitcnt vmcnt(6)
	ds_write2_b32 v41, v44, v45 offset0:48 offset1:114
	s_waitcnt vmcnt(4)
	ds_write2_b32 v41, v46, v47 offset0:180 offset1:246
	v_add_u32_e32 v41, 0x1c00, v42
	s_waitcnt vmcnt(2)
	ds_write2_b32 v41, v50, v51 offset0:56 offset1:122
	s_waitcnt vmcnt(0)
	ds_write2_b32 v41, v52, v40 offset0:188 offset1:254
	s_waitcnt lgkmcnt(0)
	ds_read2_b32 v[40:41], v43 offset0:33 offset1:41
	ds_read2_b32 v[50:51], v43 offset1:8
	ds_read2_b32 v[52:53], v43 offset0:66 offset1:74
	ds_read2_b32 v[54:55], v43 offset0:99 offset1:107
	ds_read2_b32 v[56:57], v43 offset0:132 offset1:140
	ds_read2_b32 v[58:59], v43 offset0:165 offset1:173
	ds_read2_b32 v[60:61], v43 offset0:198 offset1:206
	ds_read2_b32 v[62:63], v43 offset0:231 offset1:239
	s_lshl_b64 s[0:1], s[0:1], 1
	s_add_u32 s0, s4, s0
	s_addc_u32 s1, s5, s1
	v_lshlrev_b32_e32 v48, 1, v2
	v_lshl_add_u64 v[64:65], s[0:1], 0, v[48:49]
	s_waitcnt lgkmcnt(6)
	v_cvt_pk_bf16_f32 v44, v50, v40
	s_waitcnt lgkmcnt(4)
	v_cvt_pk_bf16_f32 v45, v52, v54
	s_waitcnt lgkmcnt(2)
	v_cvt_pk_bf16_f32 v46, v56, v58
	s_waitcnt lgkmcnt(0)
	v_cvt_pk_bf16_f32 v47, v60, v62
	v_lshl_add_u64 v[66:67], v[64:65], 0, v[28:29]
	global_store_dwordx4 v[66:67], v[44:47], off
	s_nop 1
	v_cvt_pk_bf16_f32 v44, v51, v41
	v_cvt_pk_bf16_f32 v45, v53, v55
	v_cvt_pk_bf16_f32 v46, v57, v59
	v_cvt_pk_bf16_f32 v47, v61, v63
	ds_read2_b32 v[50:51], v43 offset0:49 offset1:57
	ds_read2_b32 v[52:53], v43 offset0:16 offset1:24
	ds_read2_b32 v[54:55], v43 offset0:82 offset1:90
	ds_read2_b32 v[56:57], v43 offset0:115 offset1:123
	ds_read2_b32 v[58:59], v43 offset0:148 offset1:156
	ds_read2_b32 v[60:61], v43 offset0:181 offset1:189
	ds_read2_b32 v[62:63], v43 offset0:214 offset1:222
	ds_read2_b32 v[66:67], v43 offset0:247 offset1:255
	v_lshl_add_u64 v[40:41], v[64:65], 0, v[30:31]
	global_store_dwordx4 v[40:41], v[44:47], off
	v_lshl_add_u64 v[40:41], v[64:65], 0, v[32:33]
	s_waitcnt lgkmcnt(6)
	v_cvt_pk_bf16_f32 v44, v52, v50
	s_waitcnt lgkmcnt(4)
	v_cvt_pk_bf16_f32 v45, v54, v56
	s_waitcnt lgkmcnt(2)
	v_cvt_pk_bf16_f32 v46, v58, v60
	s_waitcnt lgkmcnt(0)
	v_cvt_pk_bf16_f32 v47, v62, v66
	global_store_dwordx4 v[40:41], v[44:47], off
	v_lshl_add_u64 v[40:41], v[64:65], 0, v[34:35]
	s_nop 0
	v_cvt_pk_bf16_f32 v44, v53, v51
	v_cvt_pk_bf16_f32 v45, v55, v57
	v_cvt_pk_bf16_f32 v46, v59, v61
	v_cvt_pk_bf16_f32 v47, v63, v67
	global_store_dwordx4 v[40:41], v[44:47], off
	s_waitcnt lgkmcnt(0)
